# speedup vs baseline: 1.1679x; 1.0095x over previous
.Lpro_nomask_A:
	v_max3_f32 v235, v64, v65, v66
	v_max3_f32 v235, v235, v67, v68
	v_max3_f32 v235, v235, v69, v70
	v_max3_f32 v235, v235, v71, v72
	v_max3_f32 v235, v235, v73, v74
	v_max3_f32 v235, v235, v75, v76
	v_max3_f32 v235, v235, v77, v78
	v_max3_f32 v235, v235, v79, v80
	v_max3_f32 v235, v235, v81, v82
	v_max3_f32 v235, v235, v83, v84
	v_max3_f32 v235, v235, v85, v86
	v_max3_f32 v235, v235, v87, v88
	v_max3_f32 v235, v235, v89, v90
	v_max3_f32 v235, v235, v91, v92
	v_max3_f32 v235, v235, v93, v94
	v_max_f32_e32 v235, v235, v95
	v_mov_b32_e32 v236, v235
	s_nop 1
	v_permlane32_swap_b32_e32 v235, v236
	v_max_f32_e32 v235, v235, v236
	v_sub_f32_e32 v96, 0, v235
	v_sub_f32_e32 v97, 0, v235
	v_sub_f32_e32 v98, 0, v235
	v_sub_f32_e32 v99, 0, v235
	v_sub_f32_e32 v100, 0, v235
	v_sub_f32_e32 v101, 0, v235
	v_sub_f32_e32 v102, 0, v235
	v_sub_f32_e32 v103, 0, v235
	v_sub_f32_e32 v104, 0, v235
	v_sub_f32_e32 v105, 0, v235
	v_sub_f32_e32 v106, 0, v235
	v_sub_f32_e32 v107, 0, v235
	v_sub_f32_e32 v108, 0, v235
	v_sub_f32_e32 v109, 0, v235
	v_sub_f32_e32 v110, 0, v235
	v_sub_f32_e32 v111, 0, v235
	v_sub_f32_e32 v64, v64, v235
	v_sub_f32_e32 v80, v80, v235
	v_sub_f32_e32 v65, v65, v235
	v_sub_f32_e32 v81, v81, v235
	v_sub_f32_e32 v66, v66, v235
	v_sub_f32_e32 v82, v82, v235
	v_sub_f32_e32 v67, v67, v235
	v_sub_f32_e32 v83, v83, v235
	v_sub_f32_e32 v68, v68, v235
	v_sub_f32_e32 v84, v84, v235
	v_sub_f32_e32 v69, v69, v235
	v_sub_f32_e32 v85, v85, v235
	v_sub_f32_e32 v70, v70, v235
	v_sub_f32_e32 v86, v86, v235
	v_sub_f32_e32 v71, v71, v235
	v_sub_f32_e32 v87, v87, v235
	v_sub_f32_e32 v72, v72, v235
	v_sub_f32_e32 v88, v88, v235
	v_sub_f32_e32 v73, v73, v235
	v_sub_f32_e32 v89, v89, v235
	v_sub_f32_e32 v74, v74, v235
	v_sub_f32_e32 v90, v90, v235
	v_sub_f32_e32 v75, v75, v235
	v_sub_f32_e32 v91, v91, v235
	v_sub_f32_e32 v76, v76, v235
	v_sub_f32_e32 v92, v92, v235
	v_sub_f32_e32 v77, v77, v235
	v_sub_f32_e32 v93, v93, v235
	v_sub_f32_e32 v78, v78, v235
	v_sub_f32_e32 v94, v94, v235
	v_sub_f32_e32 v79, v79, v235
	v_sub_f32_e32 v95, v95, v235
	v_mov_b32_e32 v0, 0
	v_mov_b32_e32 v1, 0
	v_mov_b32_e32 v2, 0
	v_mov_b32_e32 v3, 0
	v_mov_b32_e32 v4, 0
	v_mov_b32_e32 v5, 0
	v_mov_b32_e32 v6, 0
	v_mov_b32_e32 v7, 0
	v_mov_b32_e32 v8, 0
	v_mov_b32_e32 v9, 0
	v_mov_b32_e32 v10, 0
	v_mov_b32_e32 v11, 0
	v_mov_b32_e32 v12, 0
	v_mov_b32_e32 v13, 0
	v_mov_b32_e32 v14, 0
	v_mov_b32_e32 v15, 0
	v_mov_b32_e32 v16, 0
	v_mov_b32_e32 v17, 0
	v_mov_b32_e32 v18, 0
	v_mov_b32_e32 v19, 0
	v_mov_b32_e32 v20, 0
	v_mov_b32_e32 v21, 0
	v_mov_b32_e32 v22, 0
	v_mov_b32_e32 v23, 0
	v_mov_b32_e32 v24, 0
	v_mov_b32_e32 v25, 0
	v_mov_b32_e32 v26, 0
	v_mov_b32_e32 v27, 0
	v_mov_b32_e32 v28, 0
	v_mov_b32_e32 v29, 0
	v_mov_b32_e32 v30, 0
	v_mov_b32_e32 v31, 0
	v_mov_b32_e32 v232, 0
	s_cmp_lt_u32 s17, 4
	s_cbranch_scc1 .Lnoprio
	s_setprio 1
.Lnoprio:
	s_waitcnt vmcnt(8)
	v_cmp_ne_u32_e64 s[20:21], 0, v224
	s_add_u32 s31, s23, 1
	s_and_b32 s31, s31, 31
	s_lshl_b32 s31, s31, 8
	s_add_u32 s26, s31, s22
	s_add_u32 s31, s23, 3
	s_and_b32 s31, s31, 31
	s_mul_i32 s31, s31, 0xc0000
	s_add_u32 s24, s31, s18
	s_add_u32 s31, s23, 2
	s_and_b32 s31, s31, 31
	s_mul_i32 s31, s31, 0xc0000
	s_add_u32 s25, s31, s19
	s_cmp_eq_u64 s[20:21], -1
	s_cselect_b32 s34, s37, s38
	ds_read_b128 v[176:179], v225 offset:9216
	s_add_u32 s31, s29, 0xc00000
	buffer_load_dwordx4 v[32:35], v243, s[4:7], s31 offen nt
	s_add_u32 s31, s29, 0xc0c000
	buffer_load_dwordx4 v[36:39], v243, s[4:7], s31 offen nt
	buffer_load_dword v224, v230, s[8:11], s26 offen
	v_exp_f32_e32 v64, v64
	v_exp_f32_e32 v65, v65
	v_cvt_pk_f16_f32 v208, v208, v209
	v_cvt_pk_f16_f32 v209, v210, v211
	ds_read_b128 v[180:183], v225 offset:9248
	v_exp_f32_e32 v66, v66
	v_exp_f32_e32 v67, v67
	v_cvt_pk_f16_f32 v212, v212, v213
	v_cvt_pk_f16_f32 v160, v64, v65
	v_add_f32_e32 v64, v64, v65
	v_cvt_pk_f16_f32 v213, v214, v215
	ds_write_b64 v227, v[208:209] offset:18432
	ds_write_b64 v227, v[212:213] offset:23040
	ds_read_b128 v[184:187], v225 offset:9280
	v_exp_f32_e32 v68, v68
	v_exp_f32_e32 v69, v69
	v_cvt_pk_f16_f32 v161, v66, v67
	v_add_f32_e32 v66, v66, v67
	ds_read_b128 v[188:191], v225 offset:9312
	buffer_load_dwordx4 v[208:211], v229, s[4:7], s24 offen
	v_exp_f32_e32 v70, v70
	v_exp_f32_e32 v71, v71
	v_cvt_pk_f16_f32 v162, v68, v69
	v_add_f32_e32 v68, v68, v69
	v_add_f32_e32 v231, v64, v66
	ds_read_b128 v[192:195], v226 offset:0
	s_add_u32 s31, s24, 0x60000
	buffer_load_dwordx4 v[212:215], v229, s[4:7], s31 offen
	v_exp_f32_e32 v72, v72
	v_exp_f32_e32 v73, v73
	v_cvt_pk_f16_f32 v163, v70, v71
	v_add_f32_e32 v70, v70, v71
	v_add_f32_e32 v231, v231, v68
	ds_read_b128 v[196:199], v226 offset:4608
	v_exp_f32_e32 v74, v74
	v_exp_f32_e32 v75, v75
	v_cvt_pk_f16_f32 v164, v72, v73
	v_add_f32_e32 v72, v72, v73
	v_add_f32_e32 v231, v231, v70
	ds_read_b128 v[200:203], v226 offset:32
	v_exp_f32_e32 v76, v76
	v_exp_f32_e32 v77, v77
	v_cvt_pk_f16_f32 v165, v74, v75
	v_add_f32_e32 v74, v74, v75
	v_add_f32_e32 v231, v231, v72
	ds_read_b128 v[204:207], v226 offset:4640
	v_exp_f32_e32 v78, v78
	v_exp_f32_e32 v79, v79
	v_cvt_pk_f16_f32 v166, v76, v77
	v_add_f32_e32 v76, v76, v77
	v_add_f32_e32 v231, v231, v74
	v_cvt_pk_f16_f32 v167, v78, v79
	v_add_f32_e32 v78, v78, v79
	v_add_f32_e32 v231, v231, v76
	v_add_f32_e32 v231, v231, v78
	v_cmp_nge_f32_e32 vcc, s34, v231
	s_cbranch_vccnz .Lovf_a1_00
.Lovfret_a1_00:
	v_add_f32_e32 v232, v232, v231
	s_waitcnt lgkmcnt(4)
	v_mfma_f32_32x32x16_f16 v[64:79], v[176:179], v[128:131], v[96:111]
	ds_read_b128 v[176:179], v225 offset:13824
	s_waitcnt vmcnt(5)
	v_exp_f32_e32 v80, v80
	v_exp_f32_e32 v81, v81
	v_cvt_pk_f16_f32 v216, v216, v217
	v_cvt_pk_f16_f32 v217, v218, v219
	v_mfma_f32_32x32x16_f16 v[64:79], v[180:183], v[132:135], v[64:79]
	ds_read_b128 v[180:183], v225 offset:13856
	v_exp_f32_e32 v82, v82
	v_exp_f32_e32 v83, v83
	v_cvt_pk_f16_f32 v218, v220, v221
	v_cvt_pk_f16_f32 v168, v80, v81
	v_add_f32_e32 v80, v80, v81
	v_cvt_pk_f16_f32 v219, v222, v223
	v_mfma_f32_32x32x16_f16 v[64:79], v[184:187], v[136:139], v[64:79]
	ds_write_b128 v228, v[216:219] offset:9216
	ds_read_b128 v[184:187], v225 offset:13888
	v_exp_f32_e32 v84, v84
	v_exp_f32_e32 v85, v85
	v_cvt_pk_f16_f32 v169, v82, v83
	v_add_f32_e32 v82, v82, v83
	v_mfma_f32_32x32x16_f16 v[64:79], v[188:191], v[140:143], v[64:79]
	ds_read_b128 v[188:191], v225 offset:13920
	buffer_load_dword v216, v230, s[4:7], s25 offen
	s_add_u32 s31, s25, 0x3000
	buffer_load_dword v217, v230, s[4:7], s31 offen
	v_exp_f32_e32 v86, v86
	v_exp_f32_e32 v87, v87
	v_cvt_pk_f16_f32 v170, v84, v85
	v_add_f32_e32 v84, v84, v85
	v_add_f32_e32 v231, v80, v82
	s_waitcnt lgkmcnt(5)
	v_mfma_f32_32x32x16_f16 v[0:15], v[192:195], v[160:163], v[0:15]
	ds_read_b128 v[192:195], v226 offset:64
	s_add_u32 s31, s25, 0x6000
	buffer_load_dword v218, v230, s[4:7], s31 offen
	s_add_u32 s31, s25, 0x9000
	buffer_load_dword v219, v230, s[4:7], s31 offen
	v_exp_f32_e32 v88, v88
	v_exp_f32_e32 v89, v89
	v_cvt_pk_f16_f32 v171, v86, v87
	v_add_f32_e32 v86, v86, v87
	v_add_f32_e32 v231, v231, v84
	v_mfma_f32_32x32x16_f16 v[16:31], v[196:199], v[160:163], v[16:31]
	ds_read_b128 v[196:199], v226 offset:4672
	s_add_u32 s31, s25, 0x18000
	buffer_load_dword v220, v230, s[4:7], s31 offen
	s_add_u32 s31, s25, 0x1b000
	buffer_load_dword v221, v230, s[4:7], s31 offen
	v_exp_f32_e32 v90, v90
	v_exp_f32_e32 v91, v91
	v_cvt_pk_f16_f32 v172, v88, v89
	v_add_f32_e32 v88, v88, v89
	v_add_f32_e32 v231, v231, v86
	v_mfma_f32_32x32x16_f16 v[0:15], v[200:203], v[164:167], v[0:15]
	ds_read_b128 v[200:203], v226 offset:96
	s_add_u32 s31, s25, 0x1e000
	buffer_load_dword v222, v230, s[4:7], s31 offen
	v_exp_f32_e32 v92, v92
	v_exp_f32_e32 v93, v93
	v_cvt_pk_f16_f32 v173, v90, v91
	v_add_f32_e32 v90, v90, v91
	v_add_f32_e32 v231, v231, v88
	v_mfma_f32_32x32x16_f16 v[16:31], v[204:207], v[164:167], v[16:31]
	ds_read_b128 v[204:207], v226 offset:4704
	s_add_u32 s31, s25, 0x21000
	buffer_load_dword v223, v230, s[4:7], s31 offen
	v_exp_f32_e32 v94, v94
	v_exp_f32_e32 v95, v95
	v_cvt_pk_f16_f32 v174, v92, v93
	v_add_f32_e32 v92, v92, v93
	v_add_f32_e32 v231, v231, v90
	v_cvt_pk_f16_f32 v175, v94, v95
	v_add_f32_e32 v94, v94, v95
	v_add_f32_e32 v231, v231, v92
	v_add_f32_e32 v231, v231, v94
	v_cmp_nge_f32_e32 vcc, s34, v231
	s_cbranch_vccnz .Lovf_a1_01
.Lovfret_a1_01:
	v_add_f32_e32 v232, v232, v231
	s_waitcnt lgkmcnt(6)
	s_barrier
	s_add_u32 s23, s23, 1
	s_waitcnt vmcnt(8)
	v_cmp_ne_u32_e64 s[20:21], 0, v224
	s_add_u32 s31, s23, 1
	s_and_b32 s31, s31, 31
	s_lshl_b32 s31, s31, 8
	s_add_u32 s26, s31, s22
	s_add_u32 s31, s23, 3
	s_and_b32 s31, s31, 31
	s_mul_i32 s31, s31, 0xc0000
	s_add_u32 s24, s31, s18
	s_add_u32 s31, s23, 2
	s_and_b32 s31, s31, 31
	s_mul_i32 s31, s31, 0xc0000
	s_add_u32 s25, s31, s19
	s_cmp_eq_u64 s[20:21], -1
	s_cselect_b32 s34, s37, s38
	s_waitcnt lgkmcnt(4)
	v_mfma_f32_32x32x16_f16 v[80:95], v[176:179], v[128:131], v[96:111]
	ds_read_b128 v[176:179], v225 offset:18432
	s_add_u32 s31, s29, 0xc18000
	buffer_load_dwordx4 v[40:43], v243, s[4:7], s31 offen nt
	s_add_u32 s31, s29, 0xc24000
	buffer_load_dwordx4 v[44:47], v243, s[4:7], s31 offen nt
	buffer_load_dword v224, v230, s[8:11], s26 offen
	v_exp_f32_e32 v64, v64
	v_exp_f32_e32 v65, v65
	v_cvt_pk_f16_f32 v208, v208, v209
	v_cvt_pk_f16_f32 v209, v210, v211
	v_mfma_f32_32x32x16_f16 v[80:95], v[180:183], v[132:135], v[80:95]
	ds_read_b128 v[180:183], v225 offset:18464
	v_exp_f32_e32 v66, v66
	v_exp_f32_e32 v67, v67
	v_cvt_pk_f16_f32 v212, v212, v213
	v_cvt_pk_f16_f32 v160, v64, v65
	v_add_f32_e32 v64, v64, v65
	v_cvt_pk_f16_f32 v213, v214, v215
	v_mfma_f32_32x32x16_f16 v[80:95], v[184:187], v[136:139], v[80:95]
	ds_write_b64 v227, v[208:209] offset:27648
	ds_write_b64 v227, v[212:213] offset:32256
	ds_read_b128 v[184:187], v225 offset:18496
	v_exp_f32_e32 v68, v68
	v_exp_f32_e32 v69, v69
	v_cvt_pk_f16_f32 v161, v66, v67
	v_add_f32_e32 v66, v66, v67
	v_mfma_f32_32x32x16_f16 v[80:95], v[188:191], v[140:143], v[80:95]
	ds_read_b128 v[188:191], v225 offset:18528
	buffer_load_dwordx4 v[208:211], v229, s[4:7], s24 offen
	v_exp_f32_e32 v70, v70
	v_exp_f32_e32 v71, v71
	v_cvt_pk_f16_f32 v162, v68, v69
	v_add_f32_e32 v68, v68, v69
	v_add_f32_e32 v231, v64, v66
	s_waitcnt lgkmcnt(6)
	v_mfma_f32_32x32x16_f16 v[0:15], v[192:195], v[168:171], v[0:15]
	ds_read_b128 v[192:195], v226 offset:9216
	s_add_u32 s31, s24, 0x60000
	buffer_load_dwordx4 v[212:215], v229, s[4:7], s31 offen
	v_exp_f32_e32 v72, v72
	v_exp_f32_e32 v73, v73
	v_cvt_pk_f16_f32 v163, v70, v71
	v_add_f32_e32 v70, v70, v71
	v_add_f32_e32 v231, v231, v68
	v_mfma_f32_32x32x16_f16 v[16:31], v[196:199], v[168:171], v[16:31]
	ds_read_b128 v[196:199], v226 offset:13824
	v_exp_f32_e32 v74, v74
	v_exp_f32_e32 v75, v75
	v_cvt_pk_f16_f32 v164, v72, v73
	v_add_f32_e32 v72, v72, v73
	v_add_f32_e32 v231, v231, v70
	v_mfma_f32_32x32x16_f16 v[0:15], v[200:203], v[172:175], v[0:15]
	ds_read_b128 v[200:203], v226 offset:9248
	v_exp_f32_e32 v76, v76
	v_exp_f32_e32 v77, v77
	v_cvt_pk_f16_f32 v165, v74, v75
	v_add_f32_e32 v74, v74, v75
	v_add_f32_e32 v231, v231, v72
	v_mfma_f32_32x32x16_f16 v[16:31], v[204:207], v[172:175], v[16:31]
	ds_read_b128 v[204:207], v226 offset:13856
	v_exp_f32_e32 v78, v78
	v_exp_f32_e32 v79, v79
	v_cvt_pk_f16_f32 v166, v76, v77
	v_add_f32_e32 v76, v76, v77
	v_add_f32_e32 v231, v231, v74
	v_cvt_pk_f16_f32 v167, v78, v79
	v_add_f32_e32 v78, v78, v79
	v_add_f32_e32 v231, v231, v76
	v_add_f32_e32 v231, v231, v78
	v_cmp_nge_f32_e32 vcc, s34, v231
	s_cbranch_vccnz .Lovf_a1_10
.Lovfret_a1_10:
	v_add_f32_e32 v232, v232, v231
	s_waitcnt lgkmcnt(4)
	v_mfma_f32_32x32x16_f16 v[64:79], v[176:179], v[128:131], v[96:111]
	ds_read_b128 v[176:179], v225 offset:23040
	s_waitcnt vmcnt(5)
	v_exp_f32_e32 v80, v80
	v_exp_f32_e32 v81, v81
	v_cvt_pk_f16_f32 v216, v216, v217
	v_cvt_pk_f16_f32 v217, v218, v219
	v_mfma_f32_32x32x16_f16 v[64:79], v[180:183], v[132:135], v[64:79]
	ds_read_b128 v[180:183], v225 offset:23072
	v_exp_f32_e32 v82, v82
	v_exp_f32_e32 v83, v83
	v_cvt_pk_f16_f32 v218, v220, v221
	v_cvt_pk_f16_f32 v168, v80, v81
	v_add_f32_e32 v80, v80, v81
	v_cvt_pk_f16_f32 v219, v222, v223
	v_mfma_f32_32x32x16_f16 v[64:79], v[184:187], v[136:139], v[64:79]
	ds_write_b128 v228, v[216:219] offset:18432
	ds_read_b128 v[184:187], v225 offset:23104
	v_exp_f32_e32 v84, v84
	v_exp_f32_e32 v85, v85
	v_cvt_pk_f16_f32 v169, v82, v83
	v_add_f32_e32 v82, v82, v83
	v_mfma_f32_32x32x16_f16 v[64:79], v[188:191], v[140:143], v[64:79]
	ds_read_b128 v[188:191], v225 offset:23136
	buffer_load_dword v216, v230, s[4:7], s25 offen
	s_add_u32 s31, s25, 0x3000
	buffer_load_dword v217, v230, s[4:7], s31 offen
	v_exp_f32_e32 v86, v86
	v_exp_f32_e32 v87, v87
	v_cvt_pk_f16_f32 v170, v84, v85
	v_add_f32_e32 v84, v84, v85
	v_add_f32_e32 v231, v80, v82
	s_waitcnt lgkmcnt(5)
	v_mfma_f32_32x32x16_f16 v[0:15], v[192:195], v[160:163], v[0:15]
	ds_read_b128 v[192:195], v226 offset:9280
	s_add_u32 s31, s25, 0x6000
	buffer_load_dword v218, v230, s[4:7], s31 offen
	s_add_u32 s31, s25, 0x9000
	buffer_load_dword v219, v230, s[4:7], s31 offen
	v_exp_f32_e32 v88, v88
	v_exp_f32_e32 v89, v89
	v_cvt_pk_f16_f32 v171, v86, v87
	v_add_f32_e32 v86, v86, v87
	v_add_f32_e32 v231, v231, v84
	v_mfma_f32_32x32x16_f16 v[16:31], v[196:199], v[160:163], v[16:31]
	ds_read_b128 v[196:199], v226 offset:13888
	s_add_u32 s31, s25, 0x18000
	buffer_load_dword v220, v230, s[4:7], s31 offen
	s_add_u32 s31, s25, 0x1b000
	buffer_load_dword v221, v230, s[4:7], s31 offen
	v_exp_f32_e32 v90, v90
	v_exp_f32_e32 v91, v91
	v_cvt_pk_f16_f32 v172, v88, v89
	v_add_f32_e32 v88, v88, v89
	v_add_f32_e32 v231, v231, v86
	v_mfma_f32_32x32x16_f16 v[0:15], v[200:203], v[164:167], v[0:15]
	ds_read_b128 v[200:203], v226 offset:9312
	s_add_u32 s31, s25, 0x1e000
	buffer_load_dword v222, v230, s[4:7], s31 offen
	v_exp_f32_e32 v92, v92
	v_exp_f32_e32 v93, v93
	v_cvt_pk_f16_f32 v173, v90, v91
	v_add_f32_e32 v90, v90, v91
	v_add_f32_e32 v231, v231, v88
	v_mfma_f32_32x32x16_f16 v[16:31], v[204:207], v[164:167], v[16:31]
	ds_read_b128 v[204:207], v226 offset:13920
	s_add_u32 s31, s25, 0x21000
	buffer_load_dword v223, v230, s[4:7], s31 offen
	v_exp_f32_e32 v94, v94
	v_exp_f32_e32 v95, v95
	v_cvt_pk_f16_f32 v174, v92, v93
	v_add_f32_e32 v92, v92, v93
	v_add_f32_e32 v231, v231, v90
	v_cvt_pk_f16_f32 v175, v94, v95
	v_add_f32_e32 v94, v94, v95
	v_add_f32_e32 v231, v231, v92
	v_add_f32_e32 v231, v231, v94
	v_cmp_nge_f32_e32 vcc, s34, v231
	s_cbranch_vccnz .Lovf_a1_11
.Lovfret_a1_11:
	v_add_f32_e32 v232, v232, v231
	s_waitcnt lgkmcnt(6)
	s_barrier
	s_add_u32 s23, s23, 1
	s_waitcnt vmcnt(8)
	v_cmp_ne_u32_e64 s[20:21], 0, v224
	s_add_u32 s31, s23, 1
	s_and_b32 s31, s31, 31
	s_lshl_b32 s31, s31, 8
	s_add_u32 s26, s31, s22
	s_add_u32 s31, s23, 3
	s_and_b32 s31, s31, 31
	s_mul_i32 s31, s31, 0xc0000
	s_add_u32 s24, s31, s18
	s_add_u32 s31, s23, 2
	s_and_b32 s31, s31, 31
	s_mul_i32 s31, s31, 0xc0000
	s_add_u32 s25, s31, s19
	s_cmp_eq_u64 s[20:21], -1
	s_cselect_b32 s34, s37, s38
	s_waitcnt lgkmcnt(4)
	v_mfma_f32_32x32x16_f16 v[80:95], v[176:179], v[128:131], v[96:111]
	ds_read_b128 v[176:179], v225 offset:27648
	s_add_u32 s31, s29, 0xc30000
	buffer_load_dwordx4 v[48:51], v243, s[4:7], s31 offen nt
	s_add_u32 s31, s29, 0xc3c000
	buffer_load_dwordx4 v[52:55], v243, s[4:7], s31 offen nt
	buffer_load_dword v224, v230, s[8:11], s26 offen
	v_exp_f32_e32 v64, v64
	v_exp_f32_e32 v65, v65
	v_cvt_pk_f16_f32 v208, v208, v209
	v_cvt_pk_f16_f32 v209, v210, v211
	v_mfma_f32_32x32x16_f16 v[80:95], v[180:183], v[132:135], v[80:95]
	ds_read_b128 v[180:183], v225 offset:27680
	v_exp_f32_e32 v66, v66
	v_exp_f32_e32 v67, v67
	v_cvt_pk_f16_f32 v212, v212, v213
	v_cvt_pk_f16_f32 v160, v64, v65
	v_add_f32_e32 v64, v64, v65
	v_cvt_pk_f16_f32 v213, v214, v215
	v_mfma_f32_32x32x16_f16 v[80:95], v[184:187], v[136:139], v[80:95]
	ds_write_b64 v227, v[208:209] offset:0
	ds_write_b64 v227, v[212:213] offset:4608
	ds_read_b128 v[184:187], v225 offset:27712
	v_exp_f32_e32 v68, v68
	v_exp_f32_e32 v69, v69
	v_cvt_pk_f16_f32 v161, v66, v67
	v_add_f32_e32 v66, v66, v67
	v_mfma_f32_32x32x16_f16 v[80:95], v[188:191], v[140:143], v[80:95]
	ds_read_b128 v[188:191], v225 offset:27744
	buffer_load_dwordx4 v[208:211], v229, s[4:7], s24 offen
	v_exp_f32_e32 v70, v70
	v_exp_f32_e32 v71, v71
	v_cvt_pk_f16_f32 v162, v68, v69
	v_add_f32_e32 v68, v68, v69
	v_add_f32_e32 v231, v64, v66
	s_waitcnt lgkmcnt(6)
	v_mfma_f32_32x32x16_f16 v[0:15], v[192:195], v[168:171], v[0:15]
	ds_read_b128 v[192:195], v226 offset:18432
	s_add_u32 s31, s24, 0x60000
	buffer_load_dwordx4 v[212:215], v229, s[4:7], s31 offen
	v_exp_f32_e32 v72, v72
	v_exp_f32_e32 v73, v73
	v_cvt_pk_f16_f32 v163, v70, v71
	v_add_f32_e32 v70, v70, v71
	v_add_f32_e32 v231, v231, v68
	v_mfma_f32_32x32x16_f16 v[16:31], v[196:199], v[168:171], v[16:31]
	ds_read_b128 v[196:199], v226 offset:23040
	v_exp_f32_e32 v74, v74
	v_exp_f32_e32 v75, v75
	v_cvt_pk_f16_f32 v164, v72, v73
	v_add_f32_e32 v72, v72, v73
	v_add_f32_e32 v231, v231, v70
	v_mfma_f32_32x32x16_f16 v[0:15], v[200:203], v[172:175], v[0:15]
	ds_read_b128 v[200:203], v226 offset:18464
	v_exp_f32_e32 v76, v76
	v_exp_f32_e32 v77, v77
	v_cvt_pk_f16_f32 v165, v74, v75
	v_add_f32_e32 v74, v74, v75
	v_add_f32_e32 v231, v231, v72
	v_mfma_f32_32x32x16_f16 v[16:31], v[204:207], v[172:175], v[16:31]
	ds_read_b128 v[204:207], v226 offset:23072
	v_exp_f32_e32 v78, v78
	v_exp_f32_e32 v79, v79
	v_cvt_pk_f16_f32 v166, v76, v77
	v_add_f32_e32 v76, v76, v77
	v_add_f32_e32 v231, v231, v74
	v_cvt_pk_f16_f32 v167, v78, v79
	v_add_f32_e32 v78, v78, v79
	v_add_f32_e32 v231, v231, v76
	v_add_f32_e32 v231, v231, v78
	v_cmp_nge_f32_e32 vcc, s34, v231
	s_cbranch_vccnz .Lovf_a1_20
.Lovfret_a1_20:
	v_add_f32_e32 v232, v232, v231
	s_waitcnt lgkmcnt(4)
	v_mfma_f32_32x32x16_f16 v[64:79], v[176:179], v[128:131], v[96:111]
	ds_read_b128 v[176:179], v225 offset:32256
	s_waitcnt vmcnt(5)
	v_exp_f32_e32 v80, v80
	v_exp_f32_e32 v81, v81
	v_cvt_pk_f16_f32 v216, v216, v217
	v_cvt_pk_f16_f32 v217, v218, v219
	v_mfma_f32_32x32x16_f16 v[64:79], v[180:183], v[132:135], v[64:79]
	ds_read_b128 v[180:183], v225 offset:32288
	v_exp_f32_e32 v82, v82
	v_exp_f32_e32 v83, v83
	v_cvt_pk_f16_f32 v218, v220, v221
	v_cvt_pk_f16_f32 v168, v80, v81
	v_add_f32_e32 v80, v80, v81
	v_cvt_pk_f16_f32 v219, v222, v223
	v_mfma_f32_32x32x16_f16 v[64:79], v[184:187], v[136:139], v[64:79]
	ds_write_b128 v228, v[216:219] offset:27648
	ds_read_b128 v[184:187], v225 offset:32320
	v_exp_f32_e32 v84, v84
	v_exp_f32_e32 v85, v85
	v_cvt_pk_f16_f32 v169, v82, v83
	v_add_f32_e32 v82, v82, v83
	v_mfma_f32_32x32x16_f16 v[64:79], v[188:191], v[140:143], v[64:79]
	ds_read_b128 v[188:191], v225 offset:32352
	buffer_load_dword v216, v230, s[4:7], s25 offen
	s_add_u32 s31, s25, 0x3000
	buffer_load_dword v217, v230, s[4:7], s31 offen
	v_exp_f32_e32 v86, v86
	v_exp_f32_e32 v87, v87
	v_cvt_pk_f16_f32 v170, v84, v85
	v_add_f32_e32 v84, v84, v85
	v_add_f32_e32 v231, v80, v82
	s_waitcnt lgkmcnt(5)
	v_mfma_f32_32x32x16_f16 v[0:15], v[192:195], v[160:163], v[0:15]
	ds_read_b128 v[192:195], v226 offset:18496
	s_add_u32 s31, s25, 0x6000
	buffer_load_dword v218, v230, s[4:7], s31 offen
	s_add_u32 s31, s25, 0x9000
	buffer_load_dword v219, v230, s[4:7], s31 offen
	v_exp_f32_e32 v88, v88
	v_exp_f32_e32 v89, v89
	v_cvt_pk_f16_f32 v171, v86, v87
	v_add_f32_e32 v86, v86, v87
	v_add_f32_e32 v231, v231, v84
	v_mfma_f32_32x32x16_f16 v[16:31], v[196:199], v[160:163], v[16:31]
	ds_read_b128 v[196:199], v226 offset:23104
	s_add_u32 s31, s25, 0x18000
	buffer_load_dword v220, v230, s[4:7], s31 offen
	s_add_u32 s31, s25, 0x1b000
	buffer_load_dword v221, v230, s[4:7], s31 offen
	v_exp_f32_e32 v90, v90
	v_exp_f32_e32 v91, v91
	v_cvt_pk_f16_f32 v172, v88, v89
	v_add_f32_e32 v88, v88, v89
	v_add_f32_e32 v231, v231, v86
	v_mfma_f32_32x32x16_f16 v[0:15], v[200:203], v[164:167], v[0:15]
	ds_read_b128 v[200:203], v226 offset:18528
	s_add_u32 s31, s25, 0x1e000
	buffer_load_dword v222, v230, s[4:7], s31 offen
	v_exp_f32_e32 v92, v92
	v_exp_f32_e32 v93, v93
	v_cvt_pk_f16_f32 v173, v90, v91
	v_add_f32_e32 v90, v90, v91
	v_add_f32_e32 v231, v231, v88
	v_mfma_f32_32x32x16_f16 v[16:31], v[204:207], v[164:167], v[16:31]
	ds_read_b128 v[204:207], v226 offset:23136
	s_add_u32 s31, s25, 0x21000
	buffer_load_dword v223, v230, s[4:7], s31 offen
	v_exp_f32_e32 v94, v94
	v_exp_f32_e32 v95, v95
	v_cvt_pk_f16_f32 v174, v92, v93
	v_add_f32_e32 v92, v92, v93
	v_add_f32_e32 v231, v231, v90
	v_cvt_pk_f16_f32 v175, v94, v95
	v_add_f32_e32 v94, v94, v95
	v_add_f32_e32 v231, v231, v92
	v_add_f32_e32 v231, v231, v94
	v_cmp_nge_f32_e32 vcc, s34, v231
	s_cbranch_vccnz .Lovf_a1_21
.Lovfret_a1_21:
	v_add_f32_e32 v232, v232, v231
	s_waitcnt lgkmcnt(6)
	s_barrier
	s_add_u32 s23, s23, 1
	s_waitcnt vmcnt(8)
	v_cmp_ne_u32_e64 s[20:21], 0, v224
	s_add_u32 s31, s23, 1
	s_and_b32 s31, s31, 31
	s_lshl_b32 s31, s31, 8
	s_add_u32 s26, s31, s22
	s_add_u32 s31, s23, 3
	s_and_b32 s31, s31, 31
	s_mul_i32 s31, s31, 0xc0000
	s_add_u32 s24, s31, s18
	s_add_u32 s31, s23, 2
	s_and_b32 s31, s31, 31
	s_mul_i32 s31, s31, 0xc0000
	s_add_u32 s25, s31, s19
	s_cmp_eq_u64 s[20:21], -1
	s_cselect_b32 s34, s37, s38
	s_waitcnt lgkmcnt(4)
	v_mfma_f32_32x32x16_f16 v[80:95], v[176:179], v[128:131], v[96:111]
	ds_read_b128 v[176:179], v225 offset:0
	s_add_u32 s31, s29, 0xc48000
	buffer_load_dwordx4 v[56:59], v243, s[4:7], s31 offen nt
	s_add_u32 s31, s29, 0xc54000
	buffer_load_dwordx4 v[60:63], v243, s[4:7], s31 offen nt
	buffer_load_dword v224, v230, s[8:11], s26 offen
	v_exp_f32_e32 v64, v64
	v_exp_f32_e32 v65, v65
	v_cvt_pk_f16_f32 v208, v208, v209
	v_cvt_pk_f16_f32 v209, v210, v211
	v_mfma_f32_32x32x16_f16 v[80:95], v[180:183], v[132:135], v[80:95]
	ds_read_b128 v[180:183], v225 offset:32
	v_exp_f32_e32 v66, v66
	v_exp_f32_e32 v67, v67
	v_cvt_pk_f16_f32 v212, v212, v213
	v_cvt_pk_f16_f32 v160, v64, v65
	v_add_f32_e32 v64, v64, v65
	v_cvt_pk_f16_f32 v213, v214, v215
	v_mfma_f32_32x32x16_f16 v[80:95], v[184:187], v[136:139], v[80:95]
	ds_write_b64 v227, v[208:209] offset:9216
	ds_write_b64 v227, v[212:213] offset:13824
	ds_read_b128 v[184:187], v225 offset:64
	v_exp_f32_e32 v68, v68
	v_exp_f32_e32 v69, v69
	v_cvt_pk_f16_f32 v161, v66, v67
	v_add_f32_e32 v66, v66, v67
	v_mfma_f32_32x32x16_f16 v[80:95], v[188:191], v[140:143], v[80:95]
	ds_read_b128 v[188:191], v225 offset:96
	buffer_load_dwordx4 v[208:211], v229, s[4:7], s24 offen
	v_exp_f32_e32 v70, v70
	v_exp_f32_e32 v71, v71
	v_cvt_pk_f16_f32 v162, v68, v69
	v_add_f32_e32 v68, v68, v69
	v_add_f32_e32 v231, v64, v66
	s_waitcnt lgkmcnt(6)
	v_mfma_f32_32x32x16_f16 v[0:15], v[192:195], v[168:171], v[0:15]
	ds_read_b128 v[192:195], v226 offset:27648
	s_add_u32 s31, s24, 0x60000
	buffer_load_dwordx4 v[212:215], v229, s[4:7], s31 offen
	v_exp_f32_e32 v72, v72
	v_exp_f32_e32 v73, v73
	v_cvt_pk_f16_f32 v163, v70, v71
	v_add_f32_e32 v70, v70, v71
	v_add_f32_e32 v231, v231, v68
	v_mfma_f32_32x32x16_f16 v[16:31], v[196:199], v[168:171], v[16:31]
	ds_read_b128 v[196:199], v226 offset:32256
	v_exp_f32_e32 v74, v74
	v_exp_f32_e32 v75, v75
	v_cvt_pk_f16_f32 v164, v72, v73
	v_add_f32_e32 v72, v72, v73
	v_add_f32_e32 v231, v231, v70
	v_mfma_f32_32x32x16_f16 v[0:15], v[200:203], v[172:175], v[0:15]
	ds_read_b128 v[200:203], v226 offset:27680
	v_exp_f32_e32 v76, v76
	v_exp_f32_e32 v77, v77
	v_cvt_pk_f16_f32 v165, v74, v75
	v_add_f32_e32 v74, v74, v75
	v_add_f32_e32 v231, v231, v72
	v_mfma_f32_32x32x16_f16 v[16:31], v[204:207], v[172:175], v[16:31]
	ds_read_b128 v[204:207], v226 offset:32288
	v_exp_f32_e32 v78, v78
	v_exp_f32_e32 v79, v79
	v_cvt_pk_f16_f32 v166, v76, v77
	v_add_f32_e32 v76, v76, v77
	v_add_f32_e32 v231, v231, v74
	v_cvt_pk_f16_f32 v167, v78, v79
	v_add_f32_e32 v78, v78, v79
	v_add_f32_e32 v231, v231, v76
	v_add_f32_e32 v231, v231, v78
	v_cmp_nge_f32_e32 vcc, s34, v231
	s_cbranch_vccnz .Lovf_a1_30
.Lovfret_a1_30:
	v_add_f32_e32 v232, v232, v231
	s_waitcnt lgkmcnt(4)
	v_mfma_f32_32x32x16_f16 v[64:79], v[176:179], v[128:131], v[96:111]
	s_waitcnt vmcnt(5)
	v_exp_f32_e32 v80, v80
	v_exp_f32_e32 v81, v81
	v_cvt_pk_f16_f32 v216, v216, v217
	v_cvt_pk_f16_f32 v217, v218, v219
	v_mfma_f32_32x32x16_f16 v[64:79], v[180:183], v[132:135], v[64:79]
	v_exp_f32_e32 v82, v82
	v_exp_f32_e32 v83, v83
	v_cvt_pk_f16_f32 v218, v220, v221
	v_cvt_pk_f16_f32 v168, v80, v81
	v_add_f32_e32 v80, v80, v81
	v_cvt_pk_f16_f32 v219, v222, v223
	v_mfma_f32_32x32x16_f16 v[64:79], v[184:187], v[136:139], v[64:79]
	ds_write_b128 v228, v[216:219] offset:0
	v_exp_f32_e32 v84, v84
	v_exp_f32_e32 v85, v85
	v_cvt_pk_f16_f32 v169, v82, v83
	v_add_f32_e32 v82, v82, v83
	v_mfma_f32_32x32x16_f16 v[64:79], v[188:191], v[140:143], v[64:79]
	buffer_load_dword v216, v230, s[4:7], s25 offen
	s_add_u32 s31, s25, 0x3000
	buffer_load_dword v217, v230, s[4:7], s31 offen
	v_exp_f32_e32 v86, v86
	v_exp_f32_e32 v87, v87
	v_cvt_pk_f16_f32 v170, v84, v85
	v_add_f32_e32 v84, v84, v85
	v_add_f32_e32 v231, v80, v82
	s_waitcnt lgkmcnt(1)
	v_mfma_f32_32x32x16_f16 v[0:15], v[192:195], v[160:163], v[0:15]
	ds_read_b128 v[192:195], v226 offset:27712
	s_add_u32 s31, s25, 0x6000
	buffer_load_dword v218, v230, s[4:7], s31 offen
	s_add_u32 s31, s25, 0x9000
	buffer_load_dword v219, v230, s[4:7], s31 offen
	v_exp_f32_e32 v88, v88
	v_exp_f32_e32 v89, v89
	v_cvt_pk_f16_f32 v171, v86, v87
	v_add_f32_e32 v86, v86, v87
	v_add_f32_e32 v231, v231, v84
	v_mfma_f32_32x32x16_f16 v[16:31], v[196:199], v[160:163], v[16:31]
	ds_read_b128 v[196:199], v226 offset:32320
	s_add_u32 s31, s25, 0x18000
	buffer_load_dword v220, v230, s[4:7], s31 offen
	s_add_u32 s31, s25, 0x1b000
	buffer_load_dword v221, v230, s[4:7], s31 offen
	v_exp_f32_e32 v90, v90
	v_exp_f32_e32 v91, v91
	v_cvt_pk_f16_f32 v172, v88, v89
	v_add_f32_e32 v88, v88, v89
	v_add_f32_e32 v231, v231, v86
	v_mfma_f32_32x32x16_f16 v[0:15], v[200:203], v[164:167], v[0:15]
	ds_read_b128 v[200:203], v226 offset:27744
	s_add_u32 s31, s25, 0x1e000
	buffer_load_dword v222, v230, s[4:7], s31 offen
	v_exp_f32_e32 v92, v92
	v_exp_f32_e32 v93, v93
	v_cvt_pk_f16_f32 v173, v90, v91
	v_add_f32_e32 v90, v90, v91
	v_add_f32_e32 v231, v231, v88
	v_mfma_f32_32x32x16_f16 v[16:31], v[204:207], v[164:167], v[16:31]
	ds_read_b128 v[204:207], v226 offset:32352
	s_add_u32 s31, s25, 0x21000
	buffer_load_dword v223, v230, s[4:7], s31 offen
	v_exp_f32_e32 v94, v94
	v_exp_f32_e32 v95, v95
	v_cvt_pk_f16_f32 v174, v92, v93
	v_add_f32_e32 v92, v92, v93
	v_add_f32_e32 v231, v231, v90
	v_cvt_pk_f16_f32 v175, v94, v95
	v_add_f32_e32 v94, v94, v95
	v_add_f32_e32 v231, v231, v92
	v_add_f32_e32 v231, v231, v94
	v_cmp_nge_f32_e32 vcc, s34, v231
	s_cbranch_vccnz .Lovf_a1_31
.Lovfret_a1_31:
	v_add_f32_e32 v232, v232, v231
	s_waitcnt lgkmcnt(4)
	s_barrier
	s_add_u32 s23, s23, 1
	s_waitcnt lgkmcnt(0)
	v_mfma_f32_32x32x16_f16 v[0:15], v[192:195], v[168:171], v[0:15]
	v_mfma_f32_32x32x16_f16 v[16:31], v[196:199], v[168:171], v[16:31]
	v_mfma_f32_32x32x16_f16 v[0:15], v[200:203], v[172:175], v[0:15]
	v_mfma_f32_32x32x16_f16 v[16:31], v[204:207], v[172:175], v[16:31]
	s_nop 15
	s_nop 7
	s_waitcnt vmcnt(8)
	v_cmp_ne_u32_e64 s[20:21], 0, v224
	v_mul_f32_e32 v32, s36, v32
	v_mul_f32_e32 v33, s36, v33
	v_mul_f32_e32 v34, s36, v34
	v_mul_f32_e32 v35, s36, v35
	v_cvt_pk_f16_f32 v32, v32, v33
	v_cvt_pk_f16_f32 v33, v34, v35
	ds_write_b64 v239, v[32:33] offset:0
	v_mul_f32_e32 v36, s36, v36
	v_mul_f32_e32 v37, s36, v37
	v_mul_f32_e32 v38, s36, v38
	v_mul_f32_e32 v39, s36, v39
	v_cvt_pk_f16_f32 v36, v36, v37
	v_cvt_pk_f16_f32 v37, v38, v39
	ds_write_b64 v239, v[36:37] offset:576
	v_mul_f32_e32 v40, s36, v40
	v_mul_f32_e32 v41, s36, v41
	v_mul_f32_e32 v42, s36, v42
	v_mul_f32_e32 v43, s36, v43
	v_cvt_pk_f16_f32 v40, v40, v41
	v_cvt_pk_f16_f32 v41, v42, v43
	ds_write_b64 v239, v[40:41] offset:1152
	v_mul_f32_e32 v44, s36, v44
	v_mul_f32_e32 v45, s36, v45
	v_mul_f32_e32 v46, s36, v46
	v_mul_f32_e32 v47, s36, v47
	v_cvt_pk_f16_f32 v44, v44, v45
	v_cvt_pk_f16_f32 v45, v46, v47
	ds_write_b64 v239, v[44:45] offset:1728
	v_mul_f32_e32 v48, s36, v48
	v_mul_f32_e32 v49, s36, v49
	v_mul_f32_e32 v50, s36, v50
	v_mul_f32_e32 v51, s36, v51
	v_cvt_pk_f16_f32 v48, v48, v49
	v_cvt_pk_f16_f32 v49, v50, v51
	ds_write_b64 v239, v[48:49] offset:2304
	v_mul_f32_e32 v52, s36, v52
	v_mul_f32_e32 v53, s36, v53
	v_mul_f32_e32 v54, s36, v54
	v_mul_f32_e32 v55, s36, v55
	v_cvt_pk_f16_f32 v52, v52, v53
	v_cvt_pk_f16_f32 v53, v54, v55
	ds_write_b64 v239, v[52:53] offset:2880
	v_mul_f32_e32 v56, s36, v56
	v_mul_f32_e32 v57, s36, v57
	v_mul_f32_e32 v58, s36, v58
	v_mul_f32_e32 v59, s36, v59
	v_cvt_pk_f16_f32 v56, v56, v57
	v_cvt_pk_f16_f32 v57, v58, v59
	ds_write_b64 v239, v[56:57] offset:3456
	v_mul_f32_e32 v60, s36, v60
	v_mul_f32_e32 v61, s36, v61
	v_mul_f32_e32 v62, s36, v62
	v_mul_f32_e32 v63, s36, v63
	v_cvt_pk_f16_f32 v60, v60, v61
	v_cvt_pk_f16_f32 v61, v62, v63
	ds_write_b64 v239, v[60:61] offset:4032
	s_waitcnt lgkmcnt(0)
	ds_read_b128 v[144:147], v240 offset:0
	ds_read_b128 v[148:151], v240 offset:32
	ds_read_b128 v[152:155], v240 offset:64
	ds_read_b128 v[156:159], v240 offset:96
	s_waitcnt lgkmcnt(0)
	ds_read_b128 v[192:195], v225 offset:4608
	ds_read_b128 v[196:199], v225 offset:4640
	ds_read_b128 v[200:203], v225 offset:4672
	ds_read_b128 v[204:207], v225 offset:4704
	s_waitcnt lgkmcnt(0)
	v_mfma_f32_32x32x16_f16 v[160:175], v[176:179], v[144:147], 0
	v_mfma_f32_32x32x16_f16 v[160:175], v[180:183], v[148:151], v[160:175]
	v_mfma_f32_32x32x16_f16 v[160:175], v[184:187], v[152:155], v[160:175]
	v_mfma_f32_32x32x16_f16 v[160:175], v[188:191], v[156:159], v[160:175]
	v_mfma_f32_32x32x16_f16 v[80:95], v[192:195], v[144:147], 0
	v_mfma_f32_32x32x16_f16 v[80:95], v[196:199], v[148:151], v[80:95]
	v_mfma_f32_32x32x16_f16 v[80:95], v[200:203], v[152:155], v[80:95]
	v_mfma_f32_32x32x16_f16 v[80:95], v[204:207], v[156:159], v[80:95]
	s_nop 15
	s_nop 3
	s_cmp_eq_u64 s[20:21], -1
	s_cbranch_scc1 .Lpro_nomask_B
	v_lshrrev_b32_e64 v235, v234, s20
	v_bfe_u32 v236, v235, 0, 1
	v_cvt_f32_u32_e32 v236, v236
	v_sub_f32_e32 v236, 1.0, v236
	v_fmac_f32_e32 v160, s35, v236
	v_bfe_u32 v236, v235, 1, 1
	v_cvt_f32_u32_e32 v236, v236
	v_sub_f32_e32 v236, 1.0, v236
	v_fmac_f32_e32 v161, s35, v236
	v_bfe_u32 v236, v235, 2, 1
	v_cvt_f32_u32_e32 v236, v236
	v_sub_f32_e32 v236, 1.0, v236
	v_fmac_f32_e32 v162, s35, v236
	v_bfe_u32 v236, v235, 3, 1
	v_cvt_f32_u32_e32 v236, v236
	v_sub_f32_e32 v236, 1.0, v236
	v_fmac_f32_e32 v163, s35, v236
	v_bfe_u32 v236, v235, 8, 1
	v_cvt_f32_u32_e32 v236, v236
	v_sub_f32_e32 v236, 1.0, v236
	v_fmac_f32_e32 v164, s35, v236
	v_bfe_u32 v236, v235, 9, 1
	v_cvt_f32_u32_e32 v236, v236
	v_sub_f32_e32 v236, 1.0, v236
	v_fmac_f32_e32 v165, s35, v236
	v_bfe_u32 v236, v235, 10, 1
	v_cvt_f32_u32_e32 v236, v236
	v_sub_f32_e32 v236, 1.0, v236
	v_fmac_f32_e32 v166, s35, v236
	v_bfe_u32 v236, v235, 11, 1
	v_cvt_f32_u32_e32 v236, v236
	v_sub_f32_e32 v236, 1.0, v236
	v_fmac_f32_e32 v167, s35, v236
	v_bfe_u32 v236, v235, 16, 1
	v_cvt_f32_u32_e32 v236, v236
	v_sub_f32_e32 v236, 1.0, v236
	v_fmac_f32_e32 v168, s35, v236
	v_bfe_u32 v236, v235, 17, 1
	v_cvt_f32_u32_e32 v236, v236
	v_sub_f32_e32 v236, 1.0, v236
	v_fmac_f32_e32 v169, s35, v236
	v_bfe_u32 v236, v235, 18, 1
	v_cvt_f32_u32_e32 v236, v236
	v_sub_f32_e32 v236, 1.0, v236
	v_fmac_f32_e32 v170, s35, v236
	v_bfe_u32 v236, v235, 19, 1
	v_cvt_f32_u32_e32 v236, v236
	v_sub_f32_e32 v236, 1.0, v236
	v_fmac_f32_e32 v171, s35, v236
	v_bfe_u32 v236, v235, 24, 1
	v_cvt_f32_u32_e32 v236, v236
	v_sub_f32_e32 v236, 1.0, v236
	v_fmac_f32_e32 v172, s35, v236
	v_bfe_u32 v236, v235, 25, 1
	v_cvt_f32_u32_e32 v236, v236
	v_sub_f32_e32 v236, 1.0, v236
	v_fmac_f32_e32 v173, s35, v236
	v_bfe_u32 v236, v235, 26, 1
	v_cvt_f32_u32_e32 v236, v236
	v_sub_f32_e32 v236, 1.0, v236
	v_fmac_f32_e32 v174, s35, v236
	v_bfe_u32 v236, v235, 27, 1
	v_cvt_f32_u32_e32 v236, v236
	v_sub_f32_e32 v236, 1.0, v236
	v_fmac_f32_e32 v175, s35, v236
	v_lshrrev_b32_e64 v235, v234, s21
	v_bfe_u32 v236, v235, 0, 1
	v_cvt_f32_u32_e32 v236, v236
	v_sub_f32_e32 v236, 1.0, v236
	v_fmac_f32_e32 v80, s35, v236
	v_bfe_u32 v236, v235, 1, 1
	v_cvt_f32_u32_e32 v236, v236
	v_sub_f32_e32 v236, 1.0, v236
	v_fmac_f32_e32 v81, s35, v236
	v_bfe_u32 v236, v235, 2, 1
	v_cvt_f32_u32_e32 v236, v236
	v_sub_f32_e32 v236, 1.0, v236
	v_fmac_f32_e32 v82, s35, v236
	v_bfe_u32 v236, v235, 3, 1
	v_cvt_f32_u32_e32 v236, v236
	v_sub_f32_e32 v236, 1.0, v236
	v_fmac_f32_e32 v83, s35, v236
	v_bfe_u32 v236, v235, 8, 1
	v_cvt_f32_u32_e32 v236, v236
	v_sub_f32_e32 v236, 1.0, v236
	v_fmac_f32_e32 v84, s35, v236
	v_bfe_u32 v236, v235, 9, 1
	v_cvt_f32_u32_e32 v236, v236
	v_sub_f32_e32 v236, 1.0, v236
	v_fmac_f32_e32 v85, s35, v236
	v_bfe_u32 v236, v235, 10, 1
	v_cvt_f32_u32_e32 v236, v236
	v_sub_f32_e32 v236, 1.0, v236
	v_fmac_f32_e32 v86, s35, v236
	v_bfe_u32 v236, v235, 11, 1
	v_cvt_f32_u32_e32 v236, v236
	v_sub_f32_e32 v236, 1.0, v236
	v_fmac_f32_e32 v87, s35, v236
	v_bfe_u32 v236, v235, 16, 1
	v_cvt_f32_u32_e32 v236, v236
	v_sub_f32_e32 v236, 1.0, v236
	v_fmac_f32_e32 v88, s35, v236
	v_bfe_u32 v236, v235, 17, 1
	v_cvt_f32_u32_e32 v236, v236
	v_sub_f32_e32 v236, 1.0, v236
	v_fmac_f32_e32 v89, s35, v236
	v_bfe_u32 v236, v235, 18, 1
	v_cvt_f32_u32_e32 v236, v236
	v_sub_f32_e32 v236, 1.0, v236
	v_fmac_f32_e32 v90, s35, v236
	v_bfe_u32 v236, v235, 19, 1
	v_cvt_f32_u32_e32 v236, v236
	v_sub_f32_e32 v236, 1.0, v236
	v_fmac_f32_e32 v91, s35, v236
	v_bfe_u32 v236, v235, 24, 1
	v_cvt_f32_u32_e32 v236, v236
	v_sub_f32_e32 v236, 1.0, v236
	v_fmac_f32_e32 v92, s35, v236
	v_bfe_u32 v236, v235, 25, 1
	v_cvt_f32_u32_e32 v236, v236
	v_sub_f32_e32 v236, 1.0, v236
	v_fmac_f32_e32 v93, s35, v236
	v_bfe_u32 v236, v235, 26, 1
	v_cvt_f32_u32_e32 v236, v236
	v_sub_f32_e32 v236, 1.0, v236
	v_fmac_f32_e32 v94, s35, v236
	v_bfe_u32 v236, v235, 27, 1
	v_cvt_f32_u32_e32 v236, v236
	v_sub_f32_e32 v236, 1.0, v236
	v_fmac_f32_e32 v95, s35, v236

.Lovfret_b31:
	v_add_f32_e32 v233, v233, v231
	s_waitcnt lgkmcnt(6)
	s_barrier
	s_add_u32 s23, s23, 1
	s_add_u32 s27, s27, 1
	s_cmp_eq_u32 s27, 7
	s_cbranch_scc0 .Lbody
	s_nop 15
	s_nop 7
	v_mov_b32_e32 v235, v232
	v_mov_b32_e32 v236, v232
	s_nop 1
	v_permlane32_swap_b32_e32 v235, v236
	v_add_f32_e32 v236, v235, v236
	v_rcp_f32_e32 v237, v236
	s_nop 0
	v_fma_f32 v238, -v236, v237, 1.0
	v_fmac_f32_e32 v237, v238, v237
	v_mul_f32_e32 v0, v237, v0
	v_mul_f32_e32 v1, v237, v1
	v_mul_f32_e32 v2, v237, v2
	v_mul_f32_e32 v3, v237, v3
	v_mul_f32_e32 v4, v237, v4
	v_mul_f32_e32 v5, v237, v5
	v_mul_f32_e32 v6, v237, v6
	v_mul_f32_e32 v7, v237, v7
	v_mul_f32_e32 v8, v237, v8
	v_mul_f32_e32 v9, v237, v9
	v_mul_f32_e32 v10, v237, v10
	v_mul_f32_e32 v11, v237, v11
	v_mul_f32_e32 v12, v237, v12
	v_mul_f32_e32 v13, v237, v13
	v_mul_f32_e32 v14, v237, v14
	v_mul_f32_e32 v15, v237, v15
	v_mul_f32_e32 v16, v237, v16
	v_mul_f32_e32 v17, v237, v17
	v_mul_f32_e32 v18, v237, v18
	v_mul_f32_e32 v19, v237, v19
	v_mul_f32_e32 v20, v237, v20
	v_mul_f32_e32 v21, v237, v21
	v_mul_f32_e32 v22, v237, v22
	v_mul_f32_e32 v23, v237, v23
	v_mul_f32_e32 v24, v237, v24
	v_mul_f32_e32 v25, v237, v25
	v_mul_f32_e32 v26, v237, v26
	v_mul_f32_e32 v27, v237, v27
	v_mul_f32_e32 v28, v237, v28
	v_mul_f32_e32 v29, v237, v29
	v_mul_f32_e32 v30, v237, v30
	v_mul_f32_e32 v31, v237, v31
	ds_write_b128 v241, v[0:3] offset:0
	ds_write_b128 v241, v[16:19] offset:128
	ds_write_b128 v241, v[4:7] offset:32
	ds_write_b128 v241, v[20:23] offset:160
	ds_write_b128 v241, v[8:11] offset:64
	ds_write_b128 v241, v[24:27] offset:192
	ds_write_b128 v241, v[12:15] offset:96
	ds_write_b128 v241, v[28:31] offset:224
	s_waitcnt lgkmcnt(0)
	ds_read_b128 v[0:3], v242 offset:0
	ds_read_b128 v[4:7], v242 offset:1088
	ds_read_b128 v[8:11], v242 offset:2176
	ds_read_b128 v[12:15], v242 offset:3264
	ds_read_b128 v[16:19], v242 offset:4352
	ds_read_b128 v[20:23], v242 offset:5440
	ds_read_b128 v[24:27], v242 offset:6528
	ds_read_b128 v[28:31], v242 offset:7616
	s_waitcnt lgkmcnt(7)
	s_add_u32 s31, s30, 0x0
	buffer_store_dwordx4 v[0:3], v244, s[12:15], s31 offen nt sc1
	s_waitcnt lgkmcnt(6)
	s_add_u32 s31, s30, 0x4000
	buffer_store_dwordx4 v[4:7], v244, s[12:15], s31 offen nt sc1
	s_waitcnt lgkmcnt(5)
	s_add_u32 s31, s30, 0x8000
	buffer_store_dwordx4 v[8:11], v244, s[12:15], s31 offen nt sc1
	s_waitcnt lgkmcnt(4)
	s_add_u32 s31, s30, 0xc000
	buffer_store_dwordx4 v[12:15], v244, s[12:15], s31 offen nt sc1
	s_waitcnt lgkmcnt(3)
	s_add_u32 s31, s30, 0x10000
	buffer_store_dwordx4 v[16:19], v244, s[12:15], s31 offen nt sc1
	s_waitcnt lgkmcnt(2)
	s_add_u32 s31, s30, 0x14000
	buffer_store_dwordx4 v[20:23], v244, s[12:15], s31 offen nt sc1
	s_waitcnt lgkmcnt(1)
	s_add_u32 s31, s30, 0x18000
	buffer_store_dwordx4 v[24:27], v244, s[12:15], s31 offen nt sc1
	s_waitcnt lgkmcnt(0)
	s_add_u32 s31, s30, 0x1c000
	buffer_store_dwordx4 v[28:31], v244, s[12:15], s31 offen nt sc1
	s_nop 1
	s_waitcnt lgkmcnt(0)
	v_mfma_f32_32x32x16_f16 v[80:95], v[176:179], v[144:147], v[112:127]
	ds_read_b128 v[176:179], v225 offset:4608
	v_mfma_f32_32x32x16_f16 v[80:95], v[180:183], v[148:151], v[80:95]
	ds_read_b128 v[180:183], v225 offset:4640
	v_mfma_f32_32x32x16_f16 v[80:95], v[184:187], v[152:155], v[80:95]
	ds_read_b128 v[184:187], v225 offset:4672
	v_mfma_f32_32x32x16_f16 v[80:95], v[188:191], v[156:159], v[80:95]
	ds_read_b128 v[188:191], v225 offset:4704
	s_nop 15
	s_nop 3
	s_waitcnt vmcnt(8)
	v_cmp_ne_u32_e64 s[20:21], 0, v224
	s_add_u32 s31, s23, 1
	s_and_b32 s31, s31, 31
	s_lshl_b32 s31, s31, 8
	s_add_u32 s26, s31, s22
	s_add_u32 s31, s23, 3
	s_and_b32 s31, s31, 31
	s_mul_i32 s31, s31, 0xc0000
	s_add_u32 s24, s31, s18
	s_add_u32 s31, s23, 2
	s_and_b32 s31, s31, 31
	s_mul_i32 s31, s31, 0xc0000
	s_add_u32 s25, s31, s19
	s_cmp_eq_u64 s[20:21], -1
	s_cselect_b32 s34, s37, s38
	s_waitcnt lgkmcnt(0)
	v_mfma_f32_32x32x16_f16 v[64:79], v[176:179], v[144:147], v[112:127]
	ds_read_b128 v[176:179], v225 offset:9216
	buffer_load_dword v224, v230, s[8:11], s26 offen
	v_exp_f32_e32 v80, v80
	v_exp_f32_e32 v81, v81
	v_cvt_pk_f16_f32 v208, v208, v209
	v_cvt_pk_f16_f32 v209, v210, v211
	v_mfma_f32_32x32x16_f16 v[64:79], v[180:183], v[148:151], v[64:79]
	ds_read_b128 v[180:183], v225 offset:9248
	v_exp_f32_e32 v82, v82
	v_exp_f32_e32 v83, v83
	v_cvt_pk_f16_f32 v212, v212, v213
	v_cvt_pk_f16_f32 v160, v80, v81
	v_add_f32_e32 v80, v80, v81
	v_cvt_pk_f16_f32 v213, v214, v215
	v_mfma_f32_32x32x16_f16 v[64:79], v[184:187], v[152:155], v[64:79]
	ds_write_b64 v227, v[208:209] offset:18432
	ds_write_b64 v227, v[212:213] offset:23040
	ds_read_b128 v[184:187], v225 offset:9280
	v_exp_f32_e32 v84, v84
	v_exp_f32_e32 v85, v85
	v_cvt_pk_f16_f32 v161, v82, v83
	v_add_f32_e32 v82, v82, v83
	v_mfma_f32_32x32x16_f16 v[64:79], v[188:191], v[156:159], v[64:79]
	ds_read_b128 v[188:191], v225 offset:9312
	buffer_load_dwordx4 v[208:211], v229, s[4:7], s24 offen
	v_exp_f32_e32 v86, v86
	v_exp_f32_e32 v87, v87
	v_cvt_pk_f16_f32 v162, v84, v85
	v_add_f32_e32 v84, v84, v85
	v_add_f32_e32 v231, v80, v82
	s_waitcnt lgkmcnt(10)
	v_mfma_f32_32x32x16_f16 v[32:47], v[192:195], v[168:171], v[32:47]
	ds_read_b128 v[192:195], v226 offset:0
	s_add_u32 s31, s24, 0x60000
	buffer_load_dwordx4 v[212:215], v229, s[4:7], s31 offen
	v_exp_f32_e32 v88, v88
	v_exp_f32_e32 v89, v89
	v_cvt_pk_f16_f32 v163, v86, v87
	v_add_f32_e32 v86, v86, v87
	v_add_f32_e32 v231, v231, v84
	v_mfma_f32_32x32x16_f16 v[48:63], v[196:199], v[168:171], v[48:63]
	ds_read_b128 v[196:199], v226 offset:4608
	v_exp_f32_e32 v90, v90
	v_exp_f32_e32 v91, v91
	v_cvt_pk_f16_f32 v164, v88, v89
	v_add_f32_e32 v88, v88, v89
	v_add_f32_e32 v231, v231, v86
	v_mfma_f32_32x32x16_f16 v[32:47], v[200:203], v[172:175], v[32:47]
	ds_read_b128 v[200:203], v226 offset:32
	v_exp_f32_e32 v92, v92
	v_exp_f32_e32 v93, v93
	v_cvt_pk_f16_f32 v165, v90, v91
	v_add_f32_e32 v90, v90, v91
	v_add_f32_e32 v231, v231, v88
	v_mfma_f32_32x32x16_f16 v[48:63], v[204:207], v[172:175], v[48:63]
	ds_read_b128 v[204:207], v226 offset:4640
	v_exp_f32_e32 v94, v94
	v_exp_f32_e32 v95, v95
	v_cvt_pk_f16_f32 v166, v92, v93
	v_add_f32_e32 v92, v92, v93
	v_add_f32_e32 v231, v231, v90
	v_cvt_pk_f16_f32 v167, v94, v95
	v_add_f32_e32 v94, v94, v95
	v_add_f32_e32 v231, v231, v92
	v_add_f32_e32 v231, v231, v94
	v_cmp_nge_f32_e32 vcc, s34, v231
	s_cbranch_vccnz .Lovf_b1_00
.Lovfret_b1_00:
	v_add_f32_e32 v233, v233, v231
	s_waitcnt lgkmcnt(4)
	v_mfma_f32_32x32x16_f16 v[80:95], v[176:179], v[144:147], v[112:127]
	ds_read_b128 v[176:179], v225 offset:13824
	s_waitcnt vmcnt(3)
	v_exp_f32_e32 v64, v64
	v_exp_f32_e32 v65, v65
	v_cvt_pk_f16_f32 v216, v216, v217
	v_cvt_pk_f16_f32 v217, v218, v219
	v_mfma_f32_32x32x16_f16 v[80:95], v[180:183], v[148:151], v[80:95]
	ds_read_b128 v[180:183], v225 offset:13856
	v_exp_f32_e32 v66, v66
	v_exp_f32_e32 v67, v67
	v_cvt_pk_f16_f32 v218, v220, v221
	v_cvt_pk_f16_f32 v168, v64, v65
	v_add_f32_e32 v64, v64, v65
	v_cvt_pk_f16_f32 v219, v222, v223
	v_mfma_f32_32x32x16_f16 v[80:95], v[184:187], v[152:155], v[80:95]
	ds_write_b128 v228, v[216:219] offset:9216
	ds_read_b128 v[184:187], v225 offset:13888
	v_exp_f32_e32 v68, v68
	v_exp_f32_e32 v69, v69
	v_cvt_pk_f16_f32 v169, v66, v67
	v_add_f32_e32 v66, v66, v67
	v_mfma_f32_32x32x16_f16 v[80:95], v[188:191], v[156:159], v[80:95]
	ds_read_b128 v[188:191], v225 offset:13920
	buffer_load_dword v216, v230, s[4:7], s25 offen
	s_add_u32 s31, s25, 0x3000
	buffer_load_dword v217, v230, s[4:7], s31 offen
	v_exp_f32_e32 v70, v70
	v_exp_f32_e32 v71, v71
	v_cvt_pk_f16_f32 v170, v68, v69
	v_add_f32_e32 v68, v68, v69
	v_add_f32_e32 v231, v64, v66
	s_waitcnt lgkmcnt(5)
	v_mfma_f32_32x32x16_f16 v[32:47], v[192:195], v[160:163], v[32:47]
	ds_read_b128 v[192:195], v226 offset:64
	s_add_u32 s31, s25, 0x6000
	buffer_load_dword v218, v230, s[4:7], s31 offen
	s_add_u32 s31, s25, 0x9000
	buffer_load_dword v219, v230, s[4:7], s31 offen
	v_exp_f32_e32 v72, v72
	v_exp_f32_e32 v73, v73
	v_cvt_pk_f16_f32 v171, v70, v71
	v_add_f32_e32 v70, v70, v71
	v_add_f32_e32 v231, v231, v68
	v_mfma_f32_32x32x16_f16 v[48:63], v[196:199], v[160:163], v[48:63]
	ds_read_b128 v[196:199], v226 offset:4672
	s_add_u32 s31, s25, 0x18000
	buffer_load_dword v220, v230, s[4:7], s31 offen
	s_add_u32 s31, s25, 0x1b000
	buffer_load_dword v221, v230, s[4:7], s31 offen
	v_exp_f32_e32 v74, v74
	v_exp_f32_e32 v75, v75
	v_cvt_pk_f16_f32 v172, v72, v73
	v_add_f32_e32 v72, v72, v73
	v_add_f32_e32 v231, v231, v70
	v_mfma_f32_32x32x16_f16 v[32:47], v[200:203], v[164:167], v[32:47]
	ds_read_b128 v[200:203], v226 offset:96
	s_add_u32 s31, s25, 0x1e000
	buffer_load_dword v222, v230, s[4:7], s31 offen
	v_exp_f32_e32 v76, v76
	v_exp_f32_e32 v77, v77
	v_cvt_pk_f16_f32 v173, v74, v75
	v_add_f32_e32 v74, v74, v75
	v_add_f32_e32 v231, v231, v72
	v_mfma_f32_32x32x16_f16 v[48:63], v[204:207], v[164:167], v[48:63]
	ds_read_b128 v[204:207], v226 offset:4704
	s_add_u32 s31, s25, 0x21000
	buffer_load_dword v223, v230, s[4:7], s31 offen
	v_exp_f32_e32 v78, v78
	v_exp_f32_e32 v79, v79
	v_cvt_pk_f16_f32 v174, v76, v77
	v_add_f32_e32 v76, v76, v77
	v_add_f32_e32 v231, v231, v74
	v_cvt_pk_f16_f32 v175, v78, v79
	v_add_f32_e32 v78, v78, v79
	v_add_f32_e32 v231, v231, v76
	v_add_f32_e32 v231, v231, v78
	v_cmp_nge_f32_e32 vcc, s34, v231
	s_cbranch_vccnz .Lovf_b1_01
.Lovfret_b1_01:
	v_add_f32_e32 v233, v233, v231
	s_waitcnt lgkmcnt(6)
	s_barrier
	s_add_u32 s23, s23, 1
	s_waitcnt vmcnt(8)
	v_cmp_ne_u32_e64 s[20:21], 0, v224
	s_add_u32 s31, s23, 1
	s_and_b32 s31, s31, 31
	s_lshl_b32 s31, s31, 8
	s_add_u32 s26, s31, s22
	s_add_u32 s31, s23, 3
	s_and_b32 s31, s31, 31
	s_mul_i32 s31, s31, 0xc0000
	s_add_u32 s24, s31, s18
	s_add_u32 s31, s23, 2
	s_and_b32 s31, s31, 31
	s_mul_i32 s31, s31, 0xc0000
	s_add_u32 s25, s31, s19
	s_cmp_eq_u64 s[20:21], -1
	s_cselect_b32 s34, s37, s38
	s_waitcnt lgkmcnt(4)
	v_mfma_f32_32x32x16_f16 v[64:79], v[176:179], v[144:147], v[112:127]
	ds_read_b128 v[176:179], v225 offset:18432
	buffer_load_dword v224, v230, s[8:11], s26 offen
	v_exp_f32_e32 v80, v80
	v_exp_f32_e32 v81, v81
	v_cvt_pk_f16_f32 v208, v208, v209
	v_cvt_pk_f16_f32 v209, v210, v211
	v_mfma_f32_32x32x16_f16 v[64:79], v[180:183], v[148:151], v[64:79]
	ds_read_b128 v[180:183], v225 offset:18464
	v_exp_f32_e32 v82, v82
	v_exp_f32_e32 v83, v83
	v_cvt_pk_f16_f32 v212, v212, v213
	v_cvt_pk_f16_f32 v160, v80, v81
	v_add_f32_e32 v80, v80, v81
	v_cvt_pk_f16_f32 v213, v214, v215
	v_mfma_f32_32x32x16_f16 v[64:79], v[184:187], v[152:155], v[64:79]
	ds_write_b64 v227, v[208:209] offset:27648
	ds_write_b64 v227, v[212:213] offset:32256
	ds_read_b128 v[184:187], v225 offset:18496
	v_exp_f32_e32 v84, v84
	v_exp_f32_e32 v85, v85
	v_cvt_pk_f16_f32 v161, v82, v83
	v_add_f32_e32 v82, v82, v83
	v_mfma_f32_32x32x16_f16 v[64:79], v[188:191], v[156:159], v[64:79]
	ds_read_b128 v[188:191], v225 offset:18528
	buffer_load_dwordx4 v[208:211], v229, s[4:7], s24 offen
	v_exp_f32_e32 v86, v86
	v_exp_f32_e32 v87, v87
	v_cvt_pk_f16_f32 v162, v84, v85
	v_add_f32_e32 v84, v84, v85
	v_add_f32_e32 v231, v80, v82
	s_waitcnt lgkmcnt(6)
	v_mfma_f32_32x32x16_f16 v[32:47], v[192:195], v[168:171], v[32:47]
	ds_read_b128 v[192:195], v226 offset:9216
	s_add_u32 s31, s24, 0x60000
	buffer_load_dwordx4 v[212:215], v229, s[4:7], s31 offen
	v_exp_f32_e32 v88, v88
	v_exp_f32_e32 v89, v89
	v_cvt_pk_f16_f32 v163, v86, v87
	v_add_f32_e32 v86, v86, v87
	v_add_f32_e32 v231, v231, v84
	v_mfma_f32_32x32x16_f16 v[48:63], v[196:199], v[168:171], v[48:63]
	ds_read_b128 v[196:199], v226 offset:13824
	v_exp_f32_e32 v90, v90
	v_exp_f32_e32 v91, v91
	v_cvt_pk_f16_f32 v164, v88, v89
	v_add_f32_e32 v88, v88, v89
	v_add_f32_e32 v231, v231, v86
	v_mfma_f32_32x32x16_f16 v[32:47], v[200:203], v[172:175], v[32:47]
	ds_read_b128 v[200:203], v226 offset:9248
	v_exp_f32_e32 v92, v92
	v_exp_f32_e32 v93, v93
	v_cvt_pk_f16_f32 v165, v90, v91
	v_add_f32_e32 v90, v90, v91
	v_add_f32_e32 v231, v231, v88
	v_mfma_f32_32x32x16_f16 v[48:63], v[204:207], v[172:175], v[48:63]
	ds_read_b128 v[204:207], v226 offset:13856
	v_exp_f32_e32 v94, v94
	v_exp_f32_e32 v95, v95
	v_cvt_pk_f16_f32 v166, v92, v93
	v_add_f32_e32 v92, v92, v93
	v_add_f32_e32 v231, v231, v90
	v_cvt_pk_f16_f32 v167, v94, v95
	v_add_f32_e32 v94, v94, v95
	v_add_f32_e32 v231, v231, v92
	v_add_f32_e32 v231, v231, v94
	v_cmp_nge_f32_e32 vcc, s34, v231
	s_cbranch_vccnz .Lovf_b1_10
.Lovfret_b1_10:
	v_add_f32_e32 v233, v233, v231
	s_waitcnt lgkmcnt(4)
	v_mfma_f32_32x32x16_f16 v[80:95], v[176:179], v[144:147], v[112:127]
	ds_read_b128 v[176:179], v225 offset:23040
	s_waitcnt vmcnt(3)
	v_exp_f32_e32 v64, v64
	v_exp_f32_e32 v65, v65
	v_cvt_pk_f16_f32 v216, v216, v217
	v_cvt_pk_f16_f32 v217, v218, v219
	v_mfma_f32_32x32x16_f16 v[80:95], v[180:183], v[148:151], v[80:95]
	ds_read_b128 v[180:183], v225 offset:23072
	v_exp_f32_e32 v66, v66
	v_exp_f32_e32 v67, v67
	v_cvt_pk_f16_f32 v218, v220, v221
	v_cvt_pk_f16_f32 v168, v64, v65
	v_add_f32_e32 v64, v64, v65
	v_cvt_pk_f16_f32 v219, v222, v223
	v_mfma_f32_32x32x16_f16 v[80:95], v[184:187], v[152:155], v[80:95]
	ds_write_b128 v228, v[216:219] offset:18432
	ds_read_b128 v[184:187], v225 offset:23104
	v_exp_f32_e32 v68, v68
	v_exp_f32_e32 v69, v69
	v_cvt_pk_f16_f32 v169, v66, v67
	v_add_f32_e32 v66, v66, v67
	v_mfma_f32_32x32x16_f16 v[80:95], v[188:191], v[156:159], v[80:95]
	ds_read_b128 v[188:191], v225 offset:23136
	buffer_load_dword v216, v230, s[4:7], s25 offen
	s_add_u32 s31, s25, 0x3000
	buffer_load_dword v217, v230, s[4:7], s31 offen
	v_exp_f32_e32 v70, v70
	v_exp_f32_e32 v71, v71
	v_cvt_pk_f16_f32 v170, v68, v69
	v_add_f32_e32 v68, v68, v69
	v_add_f32_e32 v231, v64, v66
	s_waitcnt lgkmcnt(5)
	v_mfma_f32_32x32x16_f16 v[32:47], v[192:195], v[160:163], v[32:47]
	ds_read_b128 v[192:195], v226 offset:9280
	s_add_u32 s31, s25, 0x6000
	buffer_load_dword v218, v230, s[4:7], s31 offen
	s_add_u32 s31, s25, 0x9000
	buffer_load_dword v219, v230, s[4:7], s31 offen
	v_exp_f32_e32 v72, v72
	v_exp_f32_e32 v73, v73
	v_cvt_pk_f16_f32 v171, v70, v71
	v_add_f32_e32 v70, v70, v71
	v_add_f32_e32 v231, v231, v68
	v_mfma_f32_32x32x16_f16 v[48:63], v[196:199], v[160:163], v[48:63]
	ds_read_b128 v[196:199], v226 offset:13888
	s_add_u32 s31, s25, 0x18000
	buffer_load_dword v220, v230, s[4:7], s31 offen
	s_add_u32 s31, s25, 0x1b000
	buffer_load_dword v221, v230, s[4:7], s31 offen
	v_exp_f32_e32 v74, v74
	v_exp_f32_e32 v75, v75
	v_cvt_pk_f16_f32 v172, v72, v73
	v_add_f32_e32 v72, v72, v73
	v_add_f32_e32 v231, v231, v70
	v_mfma_f32_32x32x16_f16 v[32:47], v[200:203], v[164:167], v[32:47]
	ds_read_b128 v[200:203], v226 offset:9312
	s_add_u32 s31, s25, 0x1e000
	buffer_load_dword v222, v230, s[4:7], s31 offen
	v_exp_f32_e32 v76, v76
	v_exp_f32_e32 v77, v77
	v_cvt_pk_f16_f32 v173, v74, v75
	v_add_f32_e32 v74, v74, v75
	v_add_f32_e32 v231, v231, v72
	v_mfma_f32_32x32x16_f16 v[48:63], v[204:207], v[164:167], v[48:63]
	ds_read_b128 v[204:207], v226 offset:13920
	s_add_u32 s31, s25, 0x21000
	buffer_load_dword v223, v230, s[4:7], s31 offen
	v_exp_f32_e32 v78, v78
	v_exp_f32_e32 v79, v79
	v_cvt_pk_f16_f32 v174, v76, v77
	v_add_f32_e32 v76, v76, v77
	v_add_f32_e32 v231, v231, v74
	v_cvt_pk_f16_f32 v175, v78, v79
	v_add_f32_e32 v78, v78, v79
	v_add_f32_e32 v231, v231, v76
	v_add_f32_e32 v231, v231, v78
	v_cmp_nge_f32_e32 vcc, s34, v231
	s_cbranch_vccnz .Lovf_b1_11
.Lovfret_b1_11:
	v_add_f32_e32 v233, v233, v231
	s_waitcnt lgkmcnt(6)
	s_barrier
	s_add_u32 s23, s23, 1
	s_waitcnt vmcnt(8)
	v_cmp_ne_u32_e64 s[20:21], 0, v224
	s_add_u32 s31, s23, 1
	s_and_b32 s31, s31, 31
	s_lshl_b32 s31, s31, 8
	s_add_u32 s26, s31, s22
	s_add_u32 s31, s23, 3
	s_and_b32 s31, s31, 31
	s_mul_i32 s31, s31, 0xc0000
	s_add_u32 s24, s31, s18
	s_add_u32 s31, s23, 2
	s_and_b32 s31, s31, 31
	s_mul_i32 s31, s31, 0xc0000
	s_add_u32 s25, s31, s19
	s_cmp_eq_u64 s[20:21], -1
	s_cselect_b32 s34, s37, s38
	s_waitcnt lgkmcnt(4)
	v_mfma_f32_32x32x16_f16 v[64:79], v[176:179], v[144:147], v[112:127]
	ds_read_b128 v[176:179], v225 offset:27648
	buffer_load_dword v224, v230, s[8:11], s26 offen
	v_exp_f32_e32 v80, v80
	v_exp_f32_e32 v81, v81
	v_cvt_pk_f16_f32 v208, v208, v209
	v_cvt_pk_f16_f32 v209, v210, v211
	v_mfma_f32_32x32x16_f16 v[64:79], v[180:183], v[148:151], v[64:79]
	ds_read_b128 v[180:183], v225 offset:27680
	v_exp_f32_e32 v82, v82
	v_exp_f32_e32 v83, v83
	v_cvt_pk_f16_f32 v212, v212, v213
	v_cvt_pk_f16_f32 v160, v80, v81
	v_add_f32_e32 v80, v80, v81
	v_cvt_pk_f16_f32 v213, v214, v215
	v_mfma_f32_32x32x16_f16 v[64:79], v[184:187], v[152:155], v[64:79]
	ds_write_b64 v227, v[208:209] offset:0
	ds_write_b64 v227, v[212:213] offset:4608
	ds_read_b128 v[184:187], v225 offset:27712
	v_exp_f32_e32 v84, v84
	v_exp_f32_e32 v85, v85
	v_cvt_pk_f16_f32 v161, v82, v83
	v_add_f32_e32 v82, v82, v83
	v_mfma_f32_32x32x16_f16 v[64:79], v[188:191], v[156:159], v[64:79]
	ds_read_b128 v[188:191], v225 offset:27744
	buffer_load_dwordx4 v[208:211], v229, s[4:7], s24 offen
	v_exp_f32_e32 v86, v86
	v_exp_f32_e32 v87, v87
	v_cvt_pk_f16_f32 v162, v84, v85
	v_add_f32_e32 v84, v84, v85
	v_add_f32_e32 v231, v80, v82
	s_waitcnt lgkmcnt(6)
	v_mfma_f32_32x32x16_f16 v[32:47], v[192:195], v[168:171], v[32:47]
	ds_read_b128 v[192:195], v226 offset:18432
	s_add_u32 s31, s24, 0x60000
	buffer_load_dwordx4 v[212:215], v229, s[4:7], s31 offen
	v_exp_f32_e32 v88, v88
	v_exp_f32_e32 v89, v89
	v_cvt_pk_f16_f32 v163, v86, v87
	v_add_f32_e32 v86, v86, v87
	v_add_f32_e32 v231, v231, v84
	v_mfma_f32_32x32x16_f16 v[48:63], v[196:199], v[168:171], v[48:63]
	ds_read_b128 v[196:199], v226 offset:23040
	v_exp_f32_e32 v90, v90
	v_exp_f32_e32 v91, v91
	v_cvt_pk_f16_f32 v164, v88, v89
	v_add_f32_e32 v88, v88, v89
	v_add_f32_e32 v231, v231, v86
	v_mfma_f32_32x32x16_f16 v[32:47], v[200:203], v[172:175], v[32:47]
	ds_read_b128 v[200:203], v226 offset:18464
	v_exp_f32_e32 v92, v92
	v_exp_f32_e32 v93, v93
	v_cvt_pk_f16_f32 v165, v90, v91
	v_add_f32_e32 v90, v90, v91
	v_add_f32_e32 v231, v231, v88
	v_mfma_f32_32x32x16_f16 v[48:63], v[204:207], v[172:175], v[48:63]
	ds_read_b128 v[204:207], v226 offset:23072
	v_exp_f32_e32 v94, v94
	v_exp_f32_e32 v95, v95
	v_cvt_pk_f16_f32 v166, v92, v93
	v_add_f32_e32 v92, v92, v93
	v_add_f32_e32 v231, v231, v90
	v_cvt_pk_f16_f32 v167, v94, v95
	v_add_f32_e32 v94, v94, v95
	v_add_f32_e32 v231, v231, v92
	v_add_f32_e32 v231, v231, v94
	v_cmp_nge_f32_e32 vcc, s34, v231
	s_cbranch_vccnz .Lovf_b1_20
.Lovfret_b1_20:
	v_add_f32_e32 v233, v233, v231
	s_waitcnt lgkmcnt(4)
	v_mfma_f32_32x32x16_f16 v[80:95], v[176:179], v[144:147], v[112:127]
	ds_read_b128 v[176:179], v225 offset:32256
	s_waitcnt vmcnt(3)
	v_exp_f32_e32 v64, v64
	v_exp_f32_e32 v65, v65
	v_cvt_pk_f16_f32 v216, v216, v217
	v_cvt_pk_f16_f32 v217, v218, v219
	v_mfma_f32_32x32x16_f16 v[80:95], v[180:183], v[148:151], v[80:95]
	ds_read_b128 v[180:183], v225 offset:32288
	v_exp_f32_e32 v66, v66
	v_exp_f32_e32 v67, v67
	v_cvt_pk_f16_f32 v218, v220, v221
	v_cvt_pk_f16_f32 v168, v64, v65
	v_add_f32_e32 v64, v64, v65
	v_cvt_pk_f16_f32 v219, v222, v223
	v_mfma_f32_32x32x16_f16 v[80:95], v[184:187], v[152:155], v[80:95]
	ds_write_b128 v228, v[216:219] offset:27648
	ds_read_b128 v[184:187], v225 offset:32320
	v_exp_f32_e32 v68, v68
	v_exp_f32_e32 v69, v69
	v_cvt_pk_f16_f32 v169, v66, v67
	v_add_f32_e32 v66, v66, v67
	v_mfma_f32_32x32x16_f16 v[80:95], v[188:191], v[156:159], v[80:95]
	ds_read_b128 v[188:191], v225 offset:32352
	buffer_load_dword v216, v230, s[4:7], s25 offen
	s_add_u32 s31, s25, 0x3000
	buffer_load_dword v217, v230, s[4:7], s31 offen
	v_exp_f32_e32 v70, v70
	v_exp_f32_e32 v71, v71
	v_cvt_pk_f16_f32 v170, v68, v69
	v_add_f32_e32 v68, v68, v69
	v_add_f32_e32 v231, v64, v66
	s_waitcnt lgkmcnt(5)
	v_mfma_f32_32x32x16_f16 v[32:47], v[192:195], v[160:163], v[32:47]
	ds_read_b128 v[192:195], v226 offset:18496
	s_add_u32 s31, s25, 0x6000
	buffer_load_dword v218, v230, s[4:7], s31 offen
	s_add_u32 s31, s25, 0x9000
	buffer_load_dword v219, v230, s[4:7], s31 offen
	v_exp_f32_e32 v72, v72
	v_exp_f32_e32 v73, v73
	v_cvt_pk_f16_f32 v171, v70, v71
	v_add_f32_e32 v70, v70, v71
	v_add_f32_e32 v231, v231, v68
	v_mfma_f32_32x32x16_f16 v[48:63], v[196:199], v[160:163], v[48:63]
	ds_read_b128 v[196:199], v226 offset:23104
	s_add_u32 s31, s25, 0x18000
	buffer_load_dword v220, v230, s[4:7], s31 offen
	s_add_u32 s31, s25, 0x1b000
	buffer_load_dword v221, v230, s[4:7], s31 offen
	v_exp_f32_e32 v74, v74
	v_exp_f32_e32 v75, v75
	v_cvt_pk_f16_f32 v172, v72, v73
	v_add_f32_e32 v72, v72, v73
	v_add_f32_e32 v231, v231, v70
	v_mfma_f32_32x32x16_f16 v[32:47], v[200:203], v[164:167], v[32:47]
	ds_read_b128 v[200:203], v226 offset:18528
	s_add_u32 s31, s25, 0x1e000
	buffer_load_dword v222, v230, s[4:7], s31 offen
	v_exp_f32_e32 v76, v76
	v_exp_f32_e32 v77, v77
	v_cvt_pk_f16_f32 v173, v74, v75
	v_add_f32_e32 v74, v74, v75
	v_add_f32_e32 v231, v231, v72
	v_mfma_f32_32x32x16_f16 v[48:63], v[204:207], v[164:167], v[48:63]
	ds_read_b128 v[204:207], v226 offset:23136
	s_add_u32 s31, s25, 0x21000
	buffer_load_dword v223, v230, s[4:7], s31 offen
	v_exp_f32_e32 v78, v78
	v_exp_f32_e32 v79, v79
	v_cvt_pk_f16_f32 v174, v76, v77
	v_add_f32_e32 v76, v76, v77
	v_add_f32_e32 v231, v231, v74
	v_cvt_pk_f16_f32 v175, v78, v79
	v_add_f32_e32 v78, v78, v79
	v_add_f32_e32 v231, v231, v76
	v_add_f32_e32 v231, v231, v78
	v_cmp_nge_f32_e32 vcc, s34, v231
	s_cbranch_vccnz .Lovf_b1_21
.Lovfret_b1_21:
	v_add_f32_e32 v233, v233, v231
	s_waitcnt lgkmcnt(6)
	s_barrier
	s_add_u32 s23, s23, 1
	s_waitcnt vmcnt(8)
	v_cmp_ne_u32_e64 s[20:21], 0, v224
	s_add_u32 s31, s23, 1
	s_and_b32 s31, s31, 31
	s_lshl_b32 s31, s31, 8
	s_add_u32 s26, s31, s22
	s_add_u32 s31, s23, 3
	s_and_b32 s31, s31, 31
	s_mul_i32 s31, s31, 0xc0000
	s_add_u32 s24, s31, s18
	s_add_u32 s31, s23, 2
	s_and_b32 s31, s31, 31
	s_mul_i32 s31, s31, 0xc0000
	s_add_u32 s25, s31, s19
	s_cmp_eq_u64 s[20:21], -1
	s_cselect_b32 s34, s37, s38
	s_waitcnt lgkmcnt(4)
	v_mfma_f32_32x32x16_f16 v[64:79], v[176:179], v[144:147], v[112:127]
	ds_read_b128 v[176:179], v225 offset:0
	buffer_load_dword v224, v230, s[8:11], s26 offen
	v_exp_f32_e32 v80, v80
	v_exp_f32_e32 v81, v81
	v_cvt_pk_f16_f32 v208, v208, v209
	v_cvt_pk_f16_f32 v209, v210, v211
	v_mfma_f32_32x32x16_f16 v[64:79], v[180:183], v[148:151], v[64:79]
	ds_read_b128 v[180:183], v225 offset:32
	v_exp_f32_e32 v82, v82
	v_exp_f32_e32 v83, v83
	v_cvt_pk_f16_f32 v212, v212, v213
	v_cvt_pk_f16_f32 v160, v80, v81
	v_add_f32_e32 v80, v80, v81
	v_cvt_pk_f16_f32 v213, v214, v215
	v_mfma_f32_32x32x16_f16 v[64:79], v[184:187], v[152:155], v[64:79]
	ds_write_b64 v227, v[208:209] offset:9216
	ds_write_b64 v227, v[212:213] offset:13824
	ds_read_b128 v[184:187], v225 offset:64
	v_exp_f32_e32 v84, v84
	v_exp_f32_e32 v85, v85
	v_cvt_pk_f16_f32 v161, v82, v83
	v_add_f32_e32 v82, v82, v83
	v_mfma_f32_32x32x16_f16 v[64:79], v[188:191], v[156:159], v[64:79]
	ds_read_b128 v[188:191], v225 offset:96
	buffer_load_dwordx4 v[208:211], v229, s[4:7], s24 offen
	v_exp_f32_e32 v86, v86
	v_exp_f32_e32 v87, v87
	v_cvt_pk_f16_f32 v162, v84, v85
	v_add_f32_e32 v84, v84, v85
	v_add_f32_e32 v231, v80, v82
	s_waitcnt lgkmcnt(6)
	v_mfma_f32_32x32x16_f16 v[32:47], v[192:195], v[168:171], v[32:47]
	ds_read_b128 v[192:195], v226 offset:27648
	s_add_u32 s31, s24, 0x60000
	buffer_load_dwordx4 v[212:215], v229, s[4:7], s31 offen
	v_exp_f32_e32 v88, v88
	v_exp_f32_e32 v89, v89
	v_cvt_pk_f16_f32 v163, v86, v87
	v_add_f32_e32 v86, v86, v87
	v_add_f32_e32 v231, v231, v84
	v_mfma_f32_32x32x16_f16 v[48:63], v[196:199], v[168:171], v[48:63]
	ds_read_b128 v[196:199], v226 offset:32256
	v_exp_f32_e32 v90, v90
	v_exp_f32_e32 v91, v91
	v_cvt_pk_f16_f32 v164, v88, v89
	v_add_f32_e32 v88, v88, v89
	v_add_f32_e32 v231, v231, v86
	v_mfma_f32_32x32x16_f16 v[32:47], v[200:203], v[172:175], v[32:47]
	ds_read_b128 v[200:203], v226 offset:27680
	v_exp_f32_e32 v92, v92
	v_exp_f32_e32 v93, v93
	v_cvt_pk_f16_f32 v165, v90, v91
	v_add_f32_e32 v90, v90, v91
	v_add_f32_e32 v231, v231, v88
	v_mfma_f32_32x32x16_f16 v[48:63], v[204:207], v[172:175], v[48:63]
	ds_read_b128 v[204:207], v226 offset:32288
	v_exp_f32_e32 v94, v94
	v_exp_f32_e32 v95, v95
	v_cvt_pk_f16_f32 v166, v92, v93
	v_add_f32_e32 v92, v92, v93
	v_add_f32_e32 v231, v231, v90
	v_cvt_pk_f16_f32 v167, v94, v95
	v_add_f32_e32 v94, v94, v95
	v_add_f32_e32 v231, v231, v92
	v_add_f32_e32 v231, v231, v94
	v_cmp_nge_f32_e32 vcc, s34, v231
	s_cbranch_vccnz .Lovf_b1_30
.Lovfret_b1_30:
	v_add_f32_e32 v233, v233, v231
	s_waitcnt vmcnt(3)
	v_exp_f32_e32 v64, v64
	v_exp_f32_e32 v65, v65
	v_cvt_pk_f16_f32 v216, v216, v217
	v_cvt_pk_f16_f32 v217, v218, v219
	v_exp_f32_e32 v66, v66
	v_exp_f32_e32 v67, v67
	v_cvt_pk_f16_f32 v218, v220, v221
	v_cvt_pk_f16_f32 v168, v64, v65
	v_add_f32_e32 v64, v64, v65
	v_cvt_pk_f16_f32 v219, v222, v223
	ds_write_b128 v228, v[216:219] offset:0
	v_exp_f32_e32 v68, v68
	v_exp_f32_e32 v69, v69
	v_cvt_pk_f16_f32 v169, v66, v67
	v_add_f32_e32 v66, v66, v67
	buffer_load_dword v216, v230, s[4:7], s25 offen
	s_add_u32 s31, s25, 0x3000
	buffer_load_dword v217, v230, s[4:7], s31 offen
	v_exp_f32_e32 v70, v70
	v_exp_f32_e32 v71, v71
	v_cvt_pk_f16_f32 v170, v68, v69
	v_add_f32_e32 v68, v68, v69
	v_add_f32_e32 v231, v64, v66
	s_waitcnt lgkmcnt(1)
	v_mfma_f32_32x32x16_f16 v[32:47], v[192:195], v[160:163], v[32:47]
	ds_read_b128 v[192:195], v226 offset:27712
	s_add_u32 s31, s25, 0x6000
	buffer_load_dword v218, v230, s[4:7], s31 offen
	s_add_u32 s31, s25, 0x9000
	buffer_load_dword v219, v230, s[4:7], s31 offen
	v_exp_f32_e32 v72, v72
	v_exp_f32_e32 v73, v73
	v_cvt_pk_f16_f32 v171, v70, v71
	v_add_f32_e32 v70, v70, v71
	v_add_f32_e32 v231, v231, v68
	v_mfma_f32_32x32x16_f16 v[48:63], v[196:199], v[160:163], v[48:63]
	ds_read_b128 v[196:199], v226 offset:32320
	s_add_u32 s31, s25, 0x18000
	buffer_load_dword v220, v230, s[4:7], s31 offen
	s_add_u32 s31, s25, 0x1b000
	buffer_load_dword v221, v230, s[4:7], s31 offen
	v_exp_f32_e32 v74, v74
	v_exp_f32_e32 v75, v75
	v_cvt_pk_f16_f32 v172, v72, v73
	v_add_f32_e32 v72, v72, v73
	v_add_f32_e32 v231, v231, v70
	v_mfma_f32_32x32x16_f16 v[32:47], v[200:203], v[164:167], v[32:47]
	ds_read_b128 v[200:203], v226 offset:27744
	s_add_u32 s31, s25, 0x1e000
	buffer_load_dword v222, v230, s[4:7], s31 offen
	v_exp_f32_e32 v76, v76
	v_exp_f32_e32 v77, v77
	v_cvt_pk_f16_f32 v173, v74, v75
	v_add_f32_e32 v74, v74, v75
	v_add_f32_e32 v231, v231, v72
	v_mfma_f32_32x32x16_f16 v[48:63], v[204:207], v[164:167], v[48:63]
	ds_read_b128 v[204:207], v226 offset:32352
	s_add_u32 s31, s25, 0x21000
	buffer_load_dword v223, v230, s[4:7], s31 offen
	v_exp_f32_e32 v78, v78
	v_exp_f32_e32 v79, v79
	v_cvt_pk_f16_f32 v174, v76, v77
	v_add_f32_e32 v76, v76, v77
	v_add_f32_e32 v231, v231, v74
	v_cvt_pk_f16_f32 v175, v78, v79
	v_add_f32_e32 v78, v78, v79
	v_add_f32_e32 v231, v231, v76
	v_add_f32_e32 v231, v231, v78
	v_cmp_nge_f32_e32 vcc, s34, v231
	s_cbranch_vccnz .Lovf_b1_31
.Lovfret_b1_31:
	v_add_f32_e32 v233, v233, v231
	s_waitcnt lgkmcnt(4)
	s_barrier
	s_add_u32 s23, s23, 1
	s_waitcnt lgkmcnt(0)
	v_mfma_f32_32x32x16_f16 v[32:47], v[192:195], v[168:171], v[32:47]
	v_mfma_f32_32x32x16_f16 v[48:63], v[196:199], v[168:171], v[48:63]
	v_mfma_f32_32x32x16_f16 v[32:47], v[200:203], v[172:175], v[32:47]
	v_mfma_f32_32x32x16_f16 v[48:63], v[204:207], v[172:175], v[48:63]
	s_nop 15
	s_nop 7
	v_mov_b32_e32 v235, v233
	v_mov_b32_e32 v236, v233
	s_nop 1
	v_permlane32_swap_b32_e32 v235, v236
	v_add_f32_e32 v236, v235, v236
	v_rcp_f32_e32 v237, v236
	s_nop 0
	v_fma_f32 v238, -v236, v237, 1.0
	v_fmac_f32_e32 v237, v238, v237
	v_mul_f32_e32 v32, v237, v32
	v_mul_f32_e32 v33, v237, v33
	v_mul_f32_e32 v34, v237, v34
	v_mul_f32_e32 v35, v237, v35
	v_mul_f32_e32 v36, v237, v36
	v_mul_f32_e32 v37, v237, v37
	v_mul_f32_e32 v38, v237, v38
	v_mul_f32_e32 v39, v237, v39
	v_mul_f32_e32 v40, v237, v40
	v_mul_f32_e32 v41, v237, v41
	v_mul_f32_e32 v42, v237, v42
	v_mul_f32_e32 v43, v237, v43
	v_mul_f32_e32 v44, v237, v44
	v_mul_f32_e32 v45, v237, v45
	v_mul_f32_e32 v46, v237, v46
	v_mul_f32_e32 v47, v237, v47
	v_mul_f32_e32 v48, v237, v48
	v_mul_f32_e32 v49, v237, v49
	v_mul_f32_e32 v50, v237, v50
	v_mul_f32_e32 v51, v237, v51
	v_mul_f32_e32 v52, v237, v52
	v_mul_f32_e32 v53, v237, v53
	v_mul_f32_e32 v54, v237, v54
	v_mul_f32_e32 v55, v237, v55
	v_mul_f32_e32 v56, v237, v56
	v_mul_f32_e32 v57, v237, v57
	v_mul_f32_e32 v58, v237, v58
	v_mul_f32_e32 v59, v237, v59
	v_mul_f32_e32 v60, v237, v60
	v_mul_f32_e32 v61, v237, v61
	v_mul_f32_e32 v62, v237, v62
	v_mul_f32_e32 v63, v237, v63
	ds_write_b128 v241, v[32:35] offset:0
	ds_write_b128 v241, v[48:51] offset:128
	ds_write_b128 v241, v[36:39] offset:32
	ds_write_b128 v241, v[52:55] offset:160
	ds_write_b128 v241, v[40:43] offset:64
	ds_write_b128 v241, v[56:59] offset:192
	ds_write_b128 v241, v[44:47] offset:96
	ds_write_b128 v241, v[60:63] offset:224
	s_waitcnt lgkmcnt(0)
	ds_read_b128 v[32:35], v242 offset:0
	ds_read_b128 v[36:39], v242 offset:1088
	ds_read_b128 v[40:43], v242 offset:2176
	ds_read_b128 v[44:47], v242 offset:3264
	ds_read_b128 v[48:51], v242 offset:4352
	ds_read_b128 v[52:55], v242 offset:5440
	ds_read_b128 v[56:59], v242 offset:6528
	ds_read_b128 v[60:63], v242 offset:7616
	s_waitcnt lgkmcnt(7)
	s_add_u32 s31, s30, 0x400000
	buffer_store_dwordx4 v[32:35], v244, s[12:15], s31 offen nt sc1
	s_waitcnt lgkmcnt(6)
	s_add_u32 s31, s30, 0x404000
	buffer_store_dwordx4 v[36:39], v244, s[12:15], s31 offen nt sc1
	s_waitcnt lgkmcnt(5)
	s_add_u32 s31, s30, 0x408000
	buffer_store_dwordx4 v[40:43], v244, s[12:15], s31 offen nt sc1
	s_waitcnt lgkmcnt(4)
	s_add_u32 s31, s30, 0x40c000
	buffer_store_dwordx4 v[44:47], v244, s[12:15], s31 offen nt sc1
	s_waitcnt lgkmcnt(3)
	s_add_u32 s31, s30, 0x410000
	buffer_store_dwordx4 v[48:51], v244, s[12:15], s31 offen nt sc1
	s_waitcnt lgkmcnt(2)
	s_add_u32 s31, s30, 0x414000
	buffer_store_dwordx4 v[52:55], v244, s[12:15], s31 offen nt sc1
	s_waitcnt lgkmcnt(1)
	s_add_u32 s31, s30, 0x418000
	buffer_store_dwordx4 v[56:59], v244, s[12:15], s31 offen nt sc1
	s_waitcnt lgkmcnt(0)
	s_add_u32 s31, s30, 0x41c000
	buffer_store_dwordx4 v[60:63], v244, s[12:15], s31 offen nt sc1
	s_endpgm

.Lovfnm_a1_00:
	v_max3_f32 v235, v64, v65, v66
	v_max3_f32 v235, v235, v67, v68
	v_max3_f32 v235, v235, v69, v70
	v_max3_f32 v235, v235, v71, v72
	v_max3_f32 v235, v235, v73, v74
	v_max3_f32 v235, v235, v75, v76
	v_max3_f32 v235, v235, v77, v78
	v_max_f32_e32 v235, v235, v79
	v_mov_b32_e32 v236, v235
	s_nop 1
	v_permlane32_swap_b32_e32 v235, v236
	v_max_f32_e32 v235, v235, v236
	v_max_f32_e32 v235, 0, v235
	v_exp_f32_e64 v237, -v235
	v_sub_f32_e32 v96, v96, v235
	v_sub_f32_e32 v97, v97, v235
	v_sub_f32_e32 v98, v98, v235
	v_sub_f32_e32 v99, v99, v235
	v_sub_f32_e32 v100, v100, v235
	v_sub_f32_e32 v101, v101, v235
	v_sub_f32_e32 v102, v102, v235
	v_sub_f32_e32 v103, v103, v235
	v_sub_f32_e32 v104, v104, v235
	v_sub_f32_e32 v105, v105, v235
	v_sub_f32_e32 v106, v106, v235
	v_sub_f32_e32 v107, v107, v235
	v_sub_f32_e32 v108, v108, v235
	v_sub_f32_e32 v109, v109, v235
	v_sub_f32_e32 v110, v110, v235
	v_sub_f32_e32 v111, v111, v235
	v_mul_f32_e32 v232, v232, v237
	v_mul_f32_e32 v0, v0, v237
	v_mul_f32_e32 v1, v1, v237
	v_mul_f32_e32 v2, v2, v237
	v_mul_f32_e32 v3, v3, v237
	v_mul_f32_e32 v4, v4, v237
	v_mul_f32_e32 v5, v5, v237
	v_mul_f32_e32 v6, v6, v237
	v_mul_f32_e32 v7, v7, v237
	v_mul_f32_e32 v8, v8, v237
	v_mul_f32_e32 v9, v9, v237
	v_mul_f32_e32 v10, v10, v237
	v_mul_f32_e32 v11, v11, v237
	v_mul_f32_e32 v12, v12, v237
	v_mul_f32_e32 v13, v13, v237
	v_mul_f32_e32 v14, v14, v237
	v_mul_f32_e32 v15, v15, v237
	v_mul_f32_e32 v16, v16, v237
	v_mul_f32_e32 v17, v17, v237
	v_mul_f32_e32 v18, v18, v237
	v_mul_f32_e32 v19, v19, v237
	v_mul_f32_e32 v20, v20, v237
	v_mul_f32_e32 v21, v21, v237
	v_mul_f32_e32 v22, v22, v237
	v_mul_f32_e32 v23, v23, v237
	v_mul_f32_e32 v24, v24, v237
	v_mul_f32_e32 v25, v25, v237
	v_mul_f32_e32 v26, v26, v237
	v_mul_f32_e32 v27, v27, v237
	v_mul_f32_e32 v28, v28, v237
	v_mul_f32_e32 v29, v29, v237
	v_mul_f32_e32 v30, v30, v237
	v_mul_f32_e32 v31, v31, v237
	v_sub_f32_e32 v64, v64, v235
	v_sub_f32_e32 v80, v80, v235
	v_sub_f32_e32 v65, v65, v235
	v_sub_f32_e32 v81, v81, v235
	v_sub_f32_e32 v66, v66, v235
	v_sub_f32_e32 v82, v82, v235
	v_sub_f32_e32 v67, v67, v235
	v_sub_f32_e32 v83, v83, v235
	v_sub_f32_e32 v68, v68, v235
	v_sub_f32_e32 v84, v84, v235
	v_sub_f32_e32 v69, v69, v235
	v_sub_f32_e32 v85, v85, v235
	v_sub_f32_e32 v70, v70, v235
	v_sub_f32_e32 v86, v86, v235
	v_sub_f32_e32 v71, v71, v235
	v_sub_f32_e32 v87, v87, v235
	v_sub_f32_e32 v72, v72, v235
	v_sub_f32_e32 v88, v88, v235
	v_sub_f32_e32 v73, v73, v235
	v_sub_f32_e32 v89, v89, v235
	v_sub_f32_e32 v74, v74, v235
	v_sub_f32_e32 v90, v90, v235
	v_sub_f32_e32 v75, v75, v235
	v_sub_f32_e32 v91, v91, v235
	v_sub_f32_e32 v76, v76, v235
	v_sub_f32_e32 v92, v92, v235
	v_sub_f32_e32 v77, v77, v235
	v_sub_f32_e32 v93, v93, v235
	v_sub_f32_e32 v78, v78, v235
	v_sub_f32_e32 v94, v94, v235
	v_sub_f32_e32 v79, v79, v235
	v_sub_f32_e32 v95, v95, v235
	v_exp_f32_e32 v64, v64
	v_exp_f32_e32 v65, v65
	v_exp_f32_e32 v66, v66
	v_exp_f32_e32 v67, v67
	v_exp_f32_e32 v68, v68
	v_exp_f32_e32 v69, v69
	v_exp_f32_e32 v70, v70
	v_exp_f32_e32 v71, v71
	v_exp_f32_e32 v72, v72
	v_exp_f32_e32 v73, v73
	v_exp_f32_e32 v74, v74
	v_exp_f32_e32 v75, v75
	v_exp_f32_e32 v76, v76
	v_exp_f32_e32 v77, v77
	v_exp_f32_e32 v78, v78
	v_exp_f32_e32 v79, v79
	s_nop 0
	v_add_f32_e32 v231, v64, v65
	v_add_f32_e32 v231, v231, v66
	v_add_f32_e32 v231, v231, v67
	v_add_f32_e32 v231, v231, v68
	v_add_f32_e32 v231, v231, v69
	v_add_f32_e32 v231, v231, v70
	v_add_f32_e32 v231, v231, v71
	v_add_f32_e32 v231, v231, v72
	v_add_f32_e32 v231, v231, v73
	v_add_f32_e32 v231, v231, v74
	v_add_f32_e32 v231, v231, v75
	v_add_f32_e32 v231, v231, v76
	v_add_f32_e32 v231, v231, v77
	v_add_f32_e32 v231, v231, v78
	v_add_f32_e32 v231, v231, v79
	v_cvt_pk_f16_f32 v160, v64, v65
	v_cvt_pk_f16_f32 v161, v66, v67
	v_cvt_pk_f16_f32 v162, v68, v69
	v_cvt_pk_f16_f32 v163, v70, v71
	v_cvt_pk_f16_f32 v164, v72, v73
	v_cvt_pk_f16_f32 v165, v74, v75
	v_cvt_pk_f16_f32 v166, v76, v77
	v_cvt_pk_f16_f32 v167, v78, v79
	s_branch .Lovfret_a1_00
.Lovf_a1_01:
	s_waitcnt lgkmcnt(0)
	s_nop 15
	s_nop 15
	s_nop 15
	ds_read_b128 v[160:163], v225 offset:4608
	ds_read_b128 v[164:167], v225 offset:4640
	s_waitcnt lgkmcnt(0)
	v_mfma_f32_32x32x16_f16 v[80:95], v[160:163], v[128:131], v[96:111]
	v_mfma_f32_32x32x16_f16 v[80:95], v[164:167], v[132:135], v[80:95]
	s_nop 15
	ds_read_b128 v[160:163], v225 offset:4672
	ds_read_b128 v[164:167], v225 offset:4704
	s_waitcnt lgkmcnt(0)
	v_mfma_f32_32x32x16_f16 v[80:95], v[160:163], v[136:139], v[80:95]
	v_mfma_f32_32x32x16_f16 v[80:95], v[164:167], v[140:143], v[80:95]
	s_nop 15
	s_nop 15
	s_cmp_eq_u64 s[20:21], -1
	s_cbranch_scc1 .Lovfnm_a1_01
	v_lshrrev_b32_e64 v235, v234, s21
	v_bfe_u32 v236, v235, 0, 1
	v_cvt_f32_u32_e32 v236, v236
	v_sub_f32_e32 v236, 1.0, v236
	v_fmac_f32_e32 v80, s35, v236
	v_bfe_u32 v236, v235, 1, 1
	v_cvt_f32_u32_e32 v236, v236
	v_sub_f32_e32 v236, 1.0, v236
	v_fmac_f32_e32 v81, s35, v236
	v_bfe_u32 v236, v235, 2, 1
	v_cvt_f32_u32_e32 v236, v236
	v_sub_f32_e32 v236, 1.0, v236
	v_fmac_f32_e32 v82, s35, v236
	v_bfe_u32 v236, v235, 3, 1
	v_cvt_f32_u32_e32 v236, v236
	v_sub_f32_e32 v236, 1.0, v236
	v_fmac_f32_e32 v83, s35, v236
	v_bfe_u32 v236, v235, 8, 1
	v_cvt_f32_u32_e32 v236, v236
	v_sub_f32_e32 v236, 1.0, v236
	v_fmac_f32_e32 v84, s35, v236
	v_bfe_u32 v236, v235, 9, 1
	v_cvt_f32_u32_e32 v236, v236
	v_sub_f32_e32 v236, 1.0, v236
	v_fmac_f32_e32 v85, s35, v236
	v_bfe_u32 v236, v235, 10, 1
	v_cvt_f32_u32_e32 v236, v236
	v_sub_f32_e32 v236, 1.0, v236
	v_fmac_f32_e32 v86, s35, v236
	v_bfe_u32 v236, v235, 11, 1
	v_cvt_f32_u32_e32 v236, v236
	v_sub_f32_e32 v236, 1.0, v236
	v_fmac_f32_e32 v87, s35, v236
	v_bfe_u32 v236, v235, 16, 1
	v_cvt_f32_u32_e32 v236, v236
	v_sub_f32_e32 v236, 1.0, v236
	v_fmac_f32_e32 v88, s35, v236
	v_bfe_u32 v236, v235, 17, 1
	v_cvt_f32_u32_e32 v236, v236
	v_sub_f32_e32 v236, 1.0, v236
	v_fmac_f32_e32 v89, s35, v236
	v_bfe_u32 v236, v235, 18, 1
	v_cvt_f32_u32_e32 v236, v236
	v_sub_f32_e32 v236, 1.0, v236
	v_fmac_f32_e32 v90, s35, v236
	v_bfe_u32 v236, v235, 19, 1
	v_cvt_f32_u32_e32 v236, v236
	v_sub_f32_e32 v236, 1.0, v236
	v_fmac_f32_e32 v91, s35, v236
	v_bfe_u32 v236, v235, 24, 1
	v_cvt_f32_u32_e32 v236, v236
	v_sub_f32_e32 v236, 1.0, v236
	v_fmac_f32_e32 v92, s35, v236
	v_bfe_u32 v236, v235, 25, 1
	v_cvt_f32_u32_e32 v236, v236
	v_sub_f32_e32 v236, 1.0, v236
	v_fmac_f32_e32 v93, s35, v236
	v_bfe_u32 v236, v235, 26, 1
	v_cvt_f32_u32_e32 v236, v236
	v_sub_f32_e32 v236, 1.0, v236
	v_fmac_f32_e32 v94, s35, v236
	v_bfe_u32 v236, v235, 27, 1
	v_cvt_f32_u32_e32 v236, v236
	v_sub_f32_e32 v236, 1.0, v236
	v_fmac_f32_e32 v95, s35, v236
.Lovfnm_a1_01:
	v_max3_f32 v235, v80, v81, v82
	v_max3_f32 v235, v235, v83, v84
	v_max3_f32 v235, v235, v85, v86
	v_max3_f32 v235, v235, v87, v88
	v_max3_f32 v235, v235, v89, v90
	v_max3_f32 v235, v235, v91, v92
	v_max3_f32 v235, v235, v93, v94
	v_max_f32_e32 v235, v235, v95
	v_mov_b32_e32 v236, v235
	s_nop 1
	v_permlane32_swap_b32_e32 v235, v236
	v_max_f32_e32 v235, v235, v236
	v_max_f32_e32 v235, 0, v235
	v_exp_f32_e64 v237, -v235
	v_sub_f32_e32 v96, v96, v235
	v_sub_f32_e32 v97, v97, v235
	v_sub_f32_e32 v98, v98, v235
	v_sub_f32_e32 v99, v99, v235
	v_sub_f32_e32 v100, v100, v235
	v_sub_f32_e32 v101, v101, v235
	v_sub_f32_e32 v102, v102, v235
	v_sub_f32_e32 v103, v103, v235
	v_sub_f32_e32 v104, v104, v235
	v_sub_f32_e32 v105, v105, v235
	v_sub_f32_e32 v106, v106, v235
	v_sub_f32_e32 v107, v107, v235
	v_sub_f32_e32 v108, v108, v235
	v_sub_f32_e32 v109, v109, v235
	v_sub_f32_e32 v110, v110, v235
	v_sub_f32_e32 v111, v111, v235
	v_mul_f32_e32 v232, v232, v237
	v_mul_f32_e32 v0, v0, v237
	v_mul_f32_e32 v1, v1, v237
	v_mul_f32_e32 v2, v2, v237
	v_mul_f32_e32 v3, v3, v237
	v_mul_f32_e32 v4, v4, v237
	v_mul_f32_e32 v5, v5, v237
	v_mul_f32_e32 v6, v6, v237
	v_mul_f32_e32 v7, v7, v237
	v_mul_f32_e32 v8, v8, v237
	v_mul_f32_e32 v9, v9, v237
	v_mul_f32_e32 v10, v10, v237
	v_mul_f32_e32 v11, v11, v237
	v_mul_f32_e32 v12, v12, v237
	v_mul_f32_e32 v13, v13, v237
	v_mul_f32_e32 v14, v14, v237
	v_mul_f32_e32 v15, v15, v237
	v_mul_f32_e32 v16, v16, v237
	v_mul_f32_e32 v17, v17, v237
	v_mul_f32_e32 v18, v18, v237
	v_mul_f32_e32 v19, v19, v237
	v_mul_f32_e32 v20, v20, v237
	v_mul_f32_e32 v21, v21, v237
	v_mul_f32_e32 v22, v22, v237
	v_mul_f32_e32 v23, v23, v237
	v_mul_f32_e32 v24, v24, v237
	v_mul_f32_e32 v25, v25, v237
	v_mul_f32_e32 v26, v26, v237
	v_mul_f32_e32 v27, v27, v237
	v_mul_f32_e32 v28, v28, v237
	v_mul_f32_e32 v29, v29, v237
	v_mul_f32_e32 v30, v30, v237
	v_mul_f32_e32 v31, v31, v237
	v_sub_f32_e32 v80, v80, v235
	v_sub_f32_e32 v64, v64, v235
	v_sub_f32_e32 v81, v81, v235
	v_sub_f32_e32 v65, v65, v235
	v_sub_f32_e32 v82, v82, v235
	v_sub_f32_e32 v66, v66, v235
	v_sub_f32_e32 v83, v83, v235
	v_sub_f32_e32 v67, v67, v235
	v_sub_f32_e32 v84, v84, v235
	v_sub_f32_e32 v68, v68, v235
	v_sub_f32_e32 v85, v85, v235
	v_sub_f32_e32 v69, v69, v235
	v_sub_f32_e32 v86, v86, v235
	v_sub_f32_e32 v70, v70, v235
	v_sub_f32_e32 v87, v87, v235
	v_sub_f32_e32 v71, v71, v235
	v_sub_f32_e32 v88, v88, v235
	v_sub_f32_e32 v72, v72, v235
	v_sub_f32_e32 v89, v89, v235
	v_sub_f32_e32 v73, v73, v235
	v_sub_f32_e32 v90, v90, v235
	v_sub_f32_e32 v74, v74, v235
	v_sub_f32_e32 v91, v91, v235
	v_sub_f32_e32 v75, v75, v235
	v_sub_f32_e32 v92, v92, v235
	v_sub_f32_e32 v76, v76, v235
	v_sub_f32_e32 v93, v93, v235
	v_sub_f32_e32 v77, v77, v235
	v_sub_f32_e32 v94, v94, v235
	v_sub_f32_e32 v78, v78, v235
	v_sub_f32_e32 v95, v95, v235
	v_sub_f32_e32 v79, v79, v235
	v_exp_f32_e32 v80, v80
	v_exp_f32_e32 v81, v81
	v_exp_f32_e32 v82, v82
	v_exp_f32_e32 v83, v83
	v_exp_f32_e32 v84, v84
	v_exp_f32_e32 v85, v85
	v_exp_f32_e32 v86, v86
	v_exp_f32_e32 v87, v87
	v_exp_f32_e32 v88, v88
	v_exp_f32_e32 v89, v89
	v_exp_f32_e32 v90, v90
	v_exp_f32_e32 v91, v91
	v_exp_f32_e32 v92, v92
	v_exp_f32_e32 v93, v93
	v_exp_f32_e32 v94, v94
	v_exp_f32_e32 v95, v95
	s_nop 0
	v_add_f32_e32 v231, v80, v81
	v_add_f32_e32 v231, v231, v82
	v_add_f32_e32 v231, v231, v83
	v_add_f32_e32 v231, v231, v84
	v_add_f32_e32 v231, v231, v85
	v_add_f32_e32 v231, v231, v86
	v_add_f32_e32 v231, v231, v87
	v_add_f32_e32 v231, v231, v88
	v_add_f32_e32 v231, v231, v89
	v_add_f32_e32 v231, v231, v90
	v_add_f32_e32 v231, v231, v91
	v_add_f32_e32 v231, v231, v92
	v_add_f32_e32 v231, v231, v93
	v_add_f32_e32 v231, v231, v94
	v_add_f32_e32 v231, v231, v95
	v_cvt_pk_f16_f32 v168, v80, v81
	v_cvt_pk_f16_f32 v169, v82, v83
	v_cvt_pk_f16_f32 v170, v84, v85
	v_cvt_pk_f16_f32 v171, v86, v87
	v_cvt_pk_f16_f32 v172, v88, v89
	v_cvt_pk_f16_f32 v173, v90, v91
	v_cvt_pk_f16_f32 v174, v92, v93
	v_cvt_pk_f16_f32 v175, v94, v95
	s_branch .Lovfret_a1_01

.Lovf_a1_11:
	s_waitcnt lgkmcnt(0)
	s_nop 15
	s_nop 15
	s_nop 15
	ds_read_b128 v[160:163], v225 offset:13824
	ds_read_b128 v[164:167], v225 offset:13856
	s_waitcnt lgkmcnt(0)
	v_mfma_f32_32x32x16_f16 v[80:95], v[160:163], v[128:131], v[96:111]
	v_mfma_f32_32x32x16_f16 v[80:95], v[164:167], v[132:135], v[80:95]
	s_nop 15
	ds_read_b128 v[160:163], v225 offset:13888
	ds_read_b128 v[164:167], v225 offset:13920
	s_waitcnt lgkmcnt(0)
	v_mfma_f32_32x32x16_f16 v[80:95], v[160:163], v[136:139], v[80:95]
	v_mfma_f32_32x32x16_f16 v[80:95], v[164:167], v[140:143], v[80:95]
	s_nop 15
	s_nop 15
	s_cmp_eq_u64 s[20:21], -1
	s_cbranch_scc1 .Lovfnm_a1_11
	v_lshrrev_b32_e64 v235, v234, s21
	v_bfe_u32 v236, v235, 0, 1
	v_cvt_f32_u32_e32 v236, v236
	v_sub_f32_e32 v236, 1.0, v236
	v_fmac_f32_e32 v80, s35, v236
	v_bfe_u32 v236, v235, 1, 1
	v_cvt_f32_u32_e32 v236, v236
	v_sub_f32_e32 v236, 1.0, v236
	v_fmac_f32_e32 v81, s35, v236
	v_bfe_u32 v236, v235, 2, 1
	v_cvt_f32_u32_e32 v236, v236
	v_sub_f32_e32 v236, 1.0, v236
	v_fmac_f32_e32 v82, s35, v236
	v_bfe_u32 v236, v235, 3, 1
	v_cvt_f32_u32_e32 v236, v236
	v_sub_f32_e32 v236, 1.0, v236
	v_fmac_f32_e32 v83, s35, v236
	v_bfe_u32 v236, v235, 8, 1
	v_cvt_f32_u32_e32 v236, v236
	v_sub_f32_e32 v236, 1.0, v236
	v_fmac_f32_e32 v84, s35, v236
	v_bfe_u32 v236, v235, 9, 1
	v_cvt_f32_u32_e32 v236, v236
	v_sub_f32_e32 v236, 1.0, v236
	v_fmac_f32_e32 v85, s35, v236
	v_bfe_u32 v236, v235, 10, 1
	v_cvt_f32_u32_e32 v236, v236
	v_sub_f32_e32 v236, 1.0, v236
	v_fmac_f32_e32 v86, s35, v236
	v_bfe_u32 v236, v235, 11, 1
	v_cvt_f32_u32_e32 v236, v236
	v_sub_f32_e32 v236, 1.0, v236
	v_fmac_f32_e32 v87, s35, v236
	v_bfe_u32 v236, v235, 16, 1
	v_cvt_f32_u32_e32 v236, v236
	v_sub_f32_e32 v236, 1.0, v236
	v_fmac_f32_e32 v88, s35, v236
	v_bfe_u32 v236, v235, 17, 1
	v_cvt_f32_u32_e32 v236, v236
	v_sub_f32_e32 v236, 1.0, v236
	v_fmac_f32_e32 v89, s35, v236
	v_bfe_u32 v236, v235, 18, 1
	v_cvt_f32_u32_e32 v236, v236
	v_sub_f32_e32 v236, 1.0, v236
	v_fmac_f32_e32 v90, s35, v236
	v_bfe_u32 v236, v235, 19, 1
	v_cvt_f32_u32_e32 v236, v236
	v_sub_f32_e32 v236, 1.0, v236
	v_fmac_f32_e32 v91, s35, v236
	v_bfe_u32 v236, v235, 24, 1
	v_cvt_f32_u32_e32 v236, v236
	v_sub_f32_e32 v236, 1.0, v236
	v_fmac_f32_e32 v92, s35, v236
	v_bfe_u32 v236, v235, 25, 1
	v_cvt_f32_u32_e32 v236, v236
	v_sub_f32_e32 v236, 1.0, v236
	v_fmac_f32_e32 v93, s35, v236
	v_bfe_u32 v236, v235, 26, 1
	v_cvt_f32_u32_e32 v236, v236
	v_sub_f32_e32 v236, 1.0, v236
	v_fmac_f32_e32 v94, s35, v236
	v_bfe_u32 v236, v235, 27, 1
	v_cvt_f32_u32_e32 v236, v236
	v_sub_f32_e32 v236, 1.0, v236
	v_fmac_f32_e32 v95, s35, v236

.Lovf_a1_21:
	s_waitcnt lgkmcnt(0)
	s_nop 15
	s_nop 15
	s_nop 15
	ds_read_b128 v[160:163], v225 offset:23040
	ds_read_b128 v[164:167], v225 offset:23072
	s_waitcnt lgkmcnt(0)
	v_mfma_f32_32x32x16_f16 v[80:95], v[160:163], v[128:131], v[96:111]
	v_mfma_f32_32x32x16_f16 v[80:95], v[164:167], v[132:135], v[80:95]
	s_nop 15
	ds_read_b128 v[160:163], v225 offset:23104
	ds_read_b128 v[164:167], v225 offset:23136
	s_waitcnt lgkmcnt(0)
	v_mfma_f32_32x32x16_f16 v[80:95], v[160:163], v[136:139], v[80:95]
	v_mfma_f32_32x32x16_f16 v[80:95], v[164:167], v[140:143], v[80:95]
	s_nop 15
	s_nop 15
	s_cmp_eq_u64 s[20:21], -1
	s_cbranch_scc1 .Lovfnm_a1_21
	v_lshrrev_b32_e64 v235, v234, s21
	v_bfe_u32 v236, v235, 0, 1
	v_cvt_f32_u32_e32 v236, v236
	v_sub_f32_e32 v236, 1.0, v236
	v_fmac_f32_e32 v80, s35, v236
	v_bfe_u32 v236, v235, 1, 1
	v_cvt_f32_u32_e32 v236, v236
	v_sub_f32_e32 v236, 1.0, v236
	v_fmac_f32_e32 v81, s35, v236
	v_bfe_u32 v236, v235, 2, 1
	v_cvt_f32_u32_e32 v236, v236
	v_sub_f32_e32 v236, 1.0, v236
	v_fmac_f32_e32 v82, s35, v236
	v_bfe_u32 v236, v235, 3, 1
	v_cvt_f32_u32_e32 v236, v236
	v_sub_f32_e32 v236, 1.0, v236
	v_fmac_f32_e32 v83, s35, v236
	v_bfe_u32 v236, v235, 8, 1
	v_cvt_f32_u32_e32 v236, v236
	v_sub_f32_e32 v236, 1.0, v236
	v_fmac_f32_e32 v84, s35, v236
	v_bfe_u32 v236, v235, 9, 1
	v_cvt_f32_u32_e32 v236, v236
	v_sub_f32_e32 v236, 1.0, v236
	v_fmac_f32_e32 v85, s35, v236
	v_bfe_u32 v236, v235, 10, 1
	v_cvt_f32_u32_e32 v236, v236
	v_sub_f32_e32 v236, 1.0, v236
	v_fmac_f32_e32 v86, s35, v236
	v_bfe_u32 v236, v235, 11, 1
	v_cvt_f32_u32_e32 v236, v236
	v_sub_f32_e32 v236, 1.0, v236
	v_fmac_f32_e32 v87, s35, v236
	v_bfe_u32 v236, v235, 16, 1
	v_cvt_f32_u32_e32 v236, v236
	v_sub_f32_e32 v236, 1.0, v236
	v_fmac_f32_e32 v88, s35, v236
	v_bfe_u32 v236, v235, 17, 1
	v_cvt_f32_u32_e32 v236, v236
	v_sub_f32_e32 v236, 1.0, v236
	v_fmac_f32_e32 v89, s35, v236
	v_bfe_u32 v236, v235, 18, 1
	v_cvt_f32_u32_e32 v236, v236
	v_sub_f32_e32 v236, 1.0, v236
	v_fmac_f32_e32 v90, s35, v236
	v_bfe_u32 v236, v235, 19, 1
	v_cvt_f32_u32_e32 v236, v236
	v_sub_f32_e32 v236, 1.0, v236
	v_fmac_f32_e32 v91, s35, v236
	v_bfe_u32 v236, v235, 24, 1
	v_cvt_f32_u32_e32 v236, v236
	v_sub_f32_e32 v236, 1.0, v236
	v_fmac_f32_e32 v92, s35, v236
	v_bfe_u32 v236, v235, 25, 1
	v_cvt_f32_u32_e32 v236, v236
	v_sub_f32_e32 v236, 1.0, v236
	v_fmac_f32_e32 v93, s35, v236
	v_bfe_u32 v236, v235, 26, 1
	v_cvt_f32_u32_e32 v236, v236
	v_sub_f32_e32 v236, 1.0, v236
	v_fmac_f32_e32 v94, s35, v236
	v_bfe_u32 v236, v235, 27, 1
	v_cvt_f32_u32_e32 v236, v236
	v_sub_f32_e32 v236, 1.0, v236
	v_fmac_f32_e32 v95, s35, v236

.Lovf_a1_31:
	s_waitcnt lgkmcnt(0)
	s_nop 15
	s_nop 15
	s_nop 15
	ds_read_b128 v[160:163], v225 offset:32256
	ds_read_b128 v[164:167], v225 offset:32288
	s_waitcnt lgkmcnt(0)
	v_mfma_f32_32x32x16_f16 v[80:95], v[160:163], v[128:131], v[96:111]
	v_mfma_f32_32x32x16_f16 v[80:95], v[164:167], v[132:135], v[80:95]
	s_nop 15
	ds_read_b128 v[160:163], v225 offset:32320
	ds_read_b128 v[164:167], v225 offset:32352
	s_waitcnt lgkmcnt(0)
	v_mfma_f32_32x32x16_f16 v[80:95], v[160:163], v[136:139], v[80:95]
	v_mfma_f32_32x32x16_f16 v[80:95], v[164:167], v[140:143], v[80:95]
	s_nop 15
	s_nop 15
	s_cmp_eq_u64 s[20:21], -1
	s_cbranch_scc1 .Lovfnm_a1_31
	v_lshrrev_b32_e64 v235, v234, s21
	v_bfe_u32 v236, v235, 0, 1
	v_cvt_f32_u32_e32 v236, v236
	v_sub_f32_e32 v236, 1.0, v236
	v_fmac_f32_e32 v80, s35, v236
	v_bfe_u32 v236, v235, 1, 1
	v_cvt_f32_u32_e32 v236, v236
	v_sub_f32_e32 v236, 1.0, v236
	v_fmac_f32_e32 v81, s35, v236
	v_bfe_u32 v236, v235, 2, 1
	v_cvt_f32_u32_e32 v236, v236
	v_sub_f32_e32 v236, 1.0, v236
	v_fmac_f32_e32 v82, s35, v236
	v_bfe_u32 v236, v235, 3, 1
	v_cvt_f32_u32_e32 v236, v236
	v_sub_f32_e32 v236, 1.0, v236
	v_fmac_f32_e32 v83, s35, v236
	v_bfe_u32 v236, v235, 8, 1
	v_cvt_f32_u32_e32 v236, v236
	v_sub_f32_e32 v236, 1.0, v236
	v_fmac_f32_e32 v84, s35, v236
	v_bfe_u32 v236, v235, 9, 1
	v_cvt_f32_u32_e32 v236, v236
	v_sub_f32_e32 v236, 1.0, v236
	v_fmac_f32_e32 v85, s35, v236
	v_bfe_u32 v236, v235, 10, 1
	v_cvt_f32_u32_e32 v236, v236
	v_sub_f32_e32 v236, 1.0, v236
	v_fmac_f32_e32 v86, s35, v236
	v_bfe_u32 v236, v235, 11, 1
	v_cvt_f32_u32_e32 v236, v236
	v_sub_f32_e32 v236, 1.0, v236
	v_fmac_f32_e32 v87, s35, v236
	v_bfe_u32 v236, v235, 16, 1
	v_cvt_f32_u32_e32 v236, v236
	v_sub_f32_e32 v236, 1.0, v236
	v_fmac_f32_e32 v88, s35, v236
	v_bfe_u32 v236, v235, 17, 1
	v_cvt_f32_u32_e32 v236, v236
	v_sub_f32_e32 v236, 1.0, v236
	v_fmac_f32_e32 v89, s35, v236
	v_bfe_u32 v236, v235, 18, 1
	v_cvt_f32_u32_e32 v236, v236
	v_sub_f32_e32 v236, 1.0, v236
	v_fmac_f32_e32 v90, s35, v236
	v_bfe_u32 v236, v235, 19, 1
	v_cvt_f32_u32_e32 v236, v236
	v_sub_f32_e32 v236, 1.0, v236
	v_fmac_f32_e32 v91, s35, v236
	v_bfe_u32 v236, v235, 24, 1
	v_cvt_f32_u32_e32 v236, v236
	v_sub_f32_e32 v236, 1.0, v236
	v_fmac_f32_e32 v92, s35, v236
	v_bfe_u32 v236, v235, 25, 1
	v_cvt_f32_u32_e32 v236, v236
	v_sub_f32_e32 v236, 1.0, v236
	v_fmac_f32_e32 v93, s35, v236
	v_bfe_u32 v236, v235, 26, 1
	v_cvt_f32_u32_e32 v236, v236
	v_sub_f32_e32 v236, 1.0, v236
	v_fmac_f32_e32 v94, s35, v236
	v_bfe_u32 v236, v235, 27, 1
	v_cvt_f32_u32_e32 v236, v236
	v_sub_f32_e32 v236, 1.0, v236
	v_fmac_f32_e32 v95, s35, v236

.Lovf_b1_00:
	s_waitcnt lgkmcnt(0)
	s_nop 15
	s_nop 15
	s_nop 15
	ds_read_b128 v[168:171], v225 offset:0
	ds_read_b128 v[172:175], v225 offset:32
	s_waitcnt lgkmcnt(0)
	v_mfma_f32_32x32x16_f16 v[80:95], v[168:171], v[144:147], v[112:127]
	v_mfma_f32_32x32x16_f16 v[80:95], v[172:175], v[148:151], v[80:95]
	s_nop 15
	ds_read_b128 v[168:171], v225 offset:64
	ds_read_b128 v[172:175], v225 offset:96
	s_waitcnt lgkmcnt(0)
	v_mfma_f32_32x32x16_f16 v[80:95], v[168:171], v[152:155], v[80:95]
	v_mfma_f32_32x32x16_f16 v[80:95], v[172:175], v[156:159], v[80:95]
	s_nop 15
	s_nop 15
	s_cmp_eq_u64 s[20:21], -1
	s_cbranch_scc1 .Lovfnm_b1_00
	v_lshrrev_b32_e64 v235, v234, s20
	v_bfe_u32 v236, v235, 0, 1
	v_cvt_f32_u32_e32 v236, v236
	v_sub_f32_e32 v236, 1.0, v236
	v_fmac_f32_e32 v80, s35, v236
	v_bfe_u32 v236, v235, 1, 1
	v_cvt_f32_u32_e32 v236, v236
	v_sub_f32_e32 v236, 1.0, v236
	v_fmac_f32_e32 v81, s35, v236
	v_bfe_u32 v236, v235, 2, 1
	v_cvt_f32_u32_e32 v236, v236
	v_sub_f32_e32 v236, 1.0, v236
	v_fmac_f32_e32 v82, s35, v236
	v_bfe_u32 v236, v235, 3, 1
	v_cvt_f32_u32_e32 v236, v236
	v_sub_f32_e32 v236, 1.0, v236
	v_fmac_f32_e32 v83, s35, v236
	v_bfe_u32 v236, v235, 8, 1
	v_cvt_f32_u32_e32 v236, v236
	v_sub_f32_e32 v236, 1.0, v236
	v_fmac_f32_e32 v84, s35, v236
	v_bfe_u32 v236, v235, 9, 1
	v_cvt_f32_u32_e32 v236, v236
	v_sub_f32_e32 v236, 1.0, v236
	v_fmac_f32_e32 v85, s35, v236
	v_bfe_u32 v236, v235, 10, 1
	v_cvt_f32_u32_e32 v236, v236
	v_sub_f32_e32 v236, 1.0, v236
	v_fmac_f32_e32 v86, s35, v236
	v_bfe_u32 v236, v235, 11, 1
	v_cvt_f32_u32_e32 v236, v236
	v_sub_f32_e32 v236, 1.0, v236
	v_fmac_f32_e32 v87, s35, v236
	v_bfe_u32 v236, v235, 16, 1
	v_cvt_f32_u32_e32 v236, v236
	v_sub_f32_e32 v236, 1.0, v236
	v_fmac_f32_e32 v88, s35, v236
	v_bfe_u32 v236, v235, 17, 1
	v_cvt_f32_u32_e32 v236, v236
	v_sub_f32_e32 v236, 1.0, v236
	v_fmac_f32_e32 v89, s35, v236
	v_bfe_u32 v236, v235, 18, 1
	v_cvt_f32_u32_e32 v236, v236
	v_sub_f32_e32 v236, 1.0, v236
	v_fmac_f32_e32 v90, s35, v236
	v_bfe_u32 v236, v235, 19, 1
	v_cvt_f32_u32_e32 v236, v236
	v_sub_f32_e32 v236, 1.0, v236
	v_fmac_f32_e32 v91, s35, v236
	v_bfe_u32 v236, v235, 24, 1
	v_cvt_f32_u32_e32 v236, v236
	v_sub_f32_e32 v236, 1.0, v236
	v_fmac_f32_e32 v92, s35, v236
	v_bfe_u32 v236, v235, 25, 1
	v_cvt_f32_u32_e32 v236, v236
	v_sub_f32_e32 v236, 1.0, v236
	v_fmac_f32_e32 v93, s35, v236
	v_bfe_u32 v236, v235, 26, 1
	v_cvt_f32_u32_e32 v236, v236
	v_sub_f32_e32 v236, 1.0, v236
	v_fmac_f32_e32 v94, s35, v236
	v_bfe_u32 v236, v235, 27, 1
	v_cvt_f32_u32_e32 v236, v236
	v_sub_f32_e32 v236, 1.0, v236
	v_fmac_f32_e32 v95, s35, v236
.Lovfnm_b1_00:
	v_max3_f32 v235, v80, v81, v82
	v_max3_f32 v235, v235, v83, v84
	v_max3_f32 v235, v235, v85, v86
	v_max3_f32 v235, v235, v87, v88
	v_max3_f32 v235, v235, v89, v90
	v_max3_f32 v235, v235, v91, v92
	v_max3_f32 v235, v235, v93, v94
	v_max_f32_e32 v235, v235, v95
	v_mov_b32_e32 v236, v235
	s_nop 1
	v_permlane32_swap_b32_e32 v235, v236
	v_max_f32_e32 v235, v235, v236
	v_max_f32_e32 v235, 0, v235
	v_exp_f32_e64 v237, -v235
	v_sub_f32_e32 v112, v112, v235
	v_sub_f32_e32 v113, v113, v235
	v_sub_f32_e32 v114, v114, v235
	v_sub_f32_e32 v115, v115, v235
	v_sub_f32_e32 v116, v116, v235
	v_sub_f32_e32 v117, v117, v235
	v_sub_f32_e32 v118, v118, v235
	v_sub_f32_e32 v119, v119, v235
	v_sub_f32_e32 v120, v120, v235
	v_sub_f32_e32 v121, v121, v235
	v_sub_f32_e32 v122, v122, v235
	v_sub_f32_e32 v123, v123, v235
	v_sub_f32_e32 v124, v124, v235
	v_sub_f32_e32 v125, v125, v235
	v_sub_f32_e32 v126, v126, v235
	v_sub_f32_e32 v127, v127, v235
	v_mul_f32_e32 v233, v233, v237
	v_mul_f32_e32 v32, v32, v237
	v_mul_f32_e32 v33, v33, v237
	v_mul_f32_e32 v34, v34, v237
	v_mul_f32_e32 v35, v35, v237
	v_mul_f32_e32 v36, v36, v237
	v_mul_f32_e32 v37, v37, v237
	v_mul_f32_e32 v38, v38, v237
	v_mul_f32_e32 v39, v39, v237
	v_mul_f32_e32 v40, v40, v237
	v_mul_f32_e32 v41, v41, v237
	v_mul_f32_e32 v42, v42, v237
	v_mul_f32_e32 v43, v43, v237
	v_mul_f32_e32 v44, v44, v237
	v_mul_f32_e32 v45, v45, v237
	v_mul_f32_e32 v46, v46, v237
	v_mul_f32_e32 v47, v47, v237
	v_mul_f32_e32 v48, v48, v237
	v_mul_f32_e32 v49, v49, v237
	v_mul_f32_e32 v50, v50, v237
	v_mul_f32_e32 v51, v51, v237
	v_mul_f32_e32 v52, v52, v237
	v_mul_f32_e32 v53, v53, v237
	v_mul_f32_e32 v54, v54, v237
	v_mul_f32_e32 v55, v55, v237
	v_mul_f32_e32 v56, v56, v237
	v_mul_f32_e32 v57, v57, v237
	v_mul_f32_e32 v58, v58, v237
	v_mul_f32_e32 v59, v59, v237
	v_mul_f32_e32 v60, v60, v237
	v_mul_f32_e32 v61, v61, v237
	v_mul_f32_e32 v62, v62, v237
	v_mul_f32_e32 v63, v63, v237
	v_sub_f32_e32 v80, v80, v235
	v_sub_f32_e32 v64, v64, v235
	v_sub_f32_e32 v81, v81, v235
	v_sub_f32_e32 v65, v65, v235
	v_sub_f32_e32 v82, v82, v235
	v_sub_f32_e32 v66, v66, v235
	v_sub_f32_e32 v83, v83, v235
	v_sub_f32_e32 v67, v67, v235
	v_sub_f32_e32 v84, v84, v235
	v_sub_f32_e32 v68, v68, v235
	v_sub_f32_e32 v85, v85, v235
	v_sub_f32_e32 v69, v69, v235
	v_sub_f32_e32 v86, v86, v235
	v_sub_f32_e32 v70, v70, v235
	v_sub_f32_e32 v87, v87, v235
	v_sub_f32_e32 v71, v71, v235
	v_sub_f32_e32 v88, v88, v235
	v_sub_f32_e32 v72, v72, v235
	v_sub_f32_e32 v89, v89, v235
	v_sub_f32_e32 v73, v73, v235
	v_sub_f32_e32 v90, v90, v235
	v_sub_f32_e32 v74, v74, v235
	v_sub_f32_e32 v91, v91, v235
	v_sub_f32_e32 v75, v75, v235
	v_sub_f32_e32 v92, v92, v235
	v_sub_f32_e32 v76, v76, v235
	v_sub_f32_e32 v93, v93, v235
	v_sub_f32_e32 v77, v77, v235
	v_sub_f32_e32 v94, v94, v235
	v_sub_f32_e32 v78, v78, v235
	v_sub_f32_e32 v95, v95, v235
	v_sub_f32_e32 v79, v79, v235
	v_exp_f32_e32 v80, v80
	v_exp_f32_e32 v81, v81
	v_exp_f32_e32 v82, v82
	v_exp_f32_e32 v83, v83
	v_exp_f32_e32 v84, v84
	v_exp_f32_e32 v85, v85
	v_exp_f32_e32 v86, v86
	v_exp_f32_e32 v87, v87
	v_exp_f32_e32 v88, v88
	v_exp_f32_e32 v89, v89
	v_exp_f32_e32 v90, v90
	v_exp_f32_e32 v91, v91
	v_exp_f32_e32 v92, v92
	v_exp_f32_e32 v93, v93
	v_exp_f32_e32 v94, v94
	v_exp_f32_e32 v95, v95
	s_nop 0
	v_add_f32_e32 v231, v80, v81
	v_add_f32_e32 v231, v231, v82
	v_add_f32_e32 v231, v231, v83
	v_add_f32_e32 v231, v231, v84
	v_add_f32_e32 v231, v231, v85
	v_add_f32_e32 v231, v231, v86
	v_add_f32_e32 v231, v231, v87
	v_add_f32_e32 v231, v231, v88
	v_add_f32_e32 v231, v231, v89
	v_add_f32_e32 v231, v231, v90
	v_add_f32_e32 v231, v231, v91
	v_add_f32_e32 v231, v231, v92
	v_add_f32_e32 v231, v231, v93
	v_add_f32_e32 v231, v231, v94
	v_add_f32_e32 v231, v231, v95
	v_cvt_pk_f16_f32 v160, v80, v81
	v_cvt_pk_f16_f32 v161, v82, v83
	v_cvt_pk_f16_f32 v162, v84, v85
	v_cvt_pk_f16_f32 v163, v86, v87
	v_cvt_pk_f16_f32 v164, v88, v89
	v_cvt_pk_f16_f32 v165, v90, v91
	v_cvt_pk_f16_f32 v166, v92, v93
	v_cvt_pk_f16_f32 v167, v94, v95
	s_branch .Lovfret_b1_00
.Lovf_b1_01:
	s_waitcnt lgkmcnt(0)
	s_nop 15
	s_nop 15
	s_nop 15
	ds_read_b128 v[160:163], v225 offset:4608
	ds_read_b128 v[164:167], v225 offset:4640
	s_waitcnt lgkmcnt(0)
	v_mfma_f32_32x32x16_f16 v[64:79], v[160:163], v[144:147], v[112:127]
	v_mfma_f32_32x32x16_f16 v[64:79], v[164:167], v[148:151], v[64:79]
	s_nop 15
	ds_read_b128 v[160:163], v225 offset:4672
	ds_read_b128 v[164:167], v225 offset:4704
	s_waitcnt lgkmcnt(0)
	v_mfma_f32_32x32x16_f16 v[64:79], v[160:163], v[152:155], v[64:79]
	v_mfma_f32_32x32x16_f16 v[64:79], v[164:167], v[156:159], v[64:79]
	s_nop 15
	s_nop 15
	s_cmp_eq_u64 s[20:21], -1
	s_cbranch_scc1 .Lovfnm_b1_01
	v_lshrrev_b32_e64 v235, v234, s21
	v_bfe_u32 v236, v235, 0, 1
	v_cvt_f32_u32_e32 v236, v236
	v_sub_f32_e32 v236, 1.0, v236
	v_fmac_f32_e32 v64, s35, v236
	v_bfe_u32 v236, v235, 1, 1
	v_cvt_f32_u32_e32 v236, v236
	v_sub_f32_e32 v236, 1.0, v236
	v_fmac_f32_e32 v65, s35, v236
	v_bfe_u32 v236, v235, 2, 1
	v_cvt_f32_u32_e32 v236, v236
	v_sub_f32_e32 v236, 1.0, v236
	v_fmac_f32_e32 v66, s35, v236
	v_bfe_u32 v236, v235, 3, 1
	v_cvt_f32_u32_e32 v236, v236
	v_sub_f32_e32 v236, 1.0, v236
	v_fmac_f32_e32 v67, s35, v236
	v_bfe_u32 v236, v235, 8, 1
	v_cvt_f32_u32_e32 v236, v236
	v_sub_f32_e32 v236, 1.0, v236
	v_fmac_f32_e32 v68, s35, v236
	v_bfe_u32 v236, v235, 9, 1
	v_cvt_f32_u32_e32 v236, v236
	v_sub_f32_e32 v236, 1.0, v236
	v_fmac_f32_e32 v69, s35, v236
	v_bfe_u32 v236, v235, 10, 1
	v_cvt_f32_u32_e32 v236, v236
	v_sub_f32_e32 v236, 1.0, v236
	v_fmac_f32_e32 v70, s35, v236
	v_bfe_u32 v236, v235, 11, 1
	v_cvt_f32_u32_e32 v236, v236
	v_sub_f32_e32 v236, 1.0, v236
	v_fmac_f32_e32 v71, s35, v236
	v_bfe_u32 v236, v235, 16, 1
	v_cvt_f32_u32_e32 v236, v236
	v_sub_f32_e32 v236, 1.0, v236
	v_fmac_f32_e32 v72, s35, v236
	v_bfe_u32 v236, v235, 17, 1
	v_cvt_f32_u32_e32 v236, v236
	v_sub_f32_e32 v236, 1.0, v236
	v_fmac_f32_e32 v73, s35, v236
	v_bfe_u32 v236, v235, 18, 1
	v_cvt_f32_u32_e32 v236, v236
	v_sub_f32_e32 v236, 1.0, v236
	v_fmac_f32_e32 v74, s35, v236
	v_bfe_u32 v236, v235, 19, 1
	v_cvt_f32_u32_e32 v236, v236
	v_sub_f32_e32 v236, 1.0, v236
	v_fmac_f32_e32 v75, s35, v236
	v_bfe_u32 v236, v235, 24, 1
	v_cvt_f32_u32_e32 v236, v236
	v_sub_f32_e32 v236, 1.0, v236
	v_fmac_f32_e32 v76, s35, v236
	v_bfe_u32 v236, v235, 25, 1
	v_cvt_f32_u32_e32 v236, v236
	v_sub_f32_e32 v236, 1.0, v236
	v_fmac_f32_e32 v77, s35, v236
	v_bfe_u32 v236, v235, 26, 1
	v_cvt_f32_u32_e32 v236, v236
	v_sub_f32_e32 v236, 1.0, v236
	v_fmac_f32_e32 v78, s35, v236
	v_bfe_u32 v236, v235, 27, 1
	v_cvt_f32_u32_e32 v236, v236
	v_sub_f32_e32 v236, 1.0, v236
	v_fmac_f32_e32 v79, s35, v236
.Lovfnm_b1_01:
	v_max3_f32 v235, v64, v65, v66
	v_max3_f32 v235, v235, v67, v68
	v_max3_f32 v235, v235, v69, v70
	v_max3_f32 v235, v235, v71, v72
	v_max3_f32 v235, v235, v73, v74
	v_max3_f32 v235, v235, v75, v76
	v_max3_f32 v235, v235, v77, v78
	v_max_f32_e32 v235, v235, v79
	v_mov_b32_e32 v236, v235
	s_nop 1
	v_permlane32_swap_b32_e32 v235, v236
	v_max_f32_e32 v235, v235, v236
	v_max_f32_e32 v235, 0, v235
	v_exp_f32_e64 v237, -v235
	v_sub_f32_e32 v112, v112, v235
	v_sub_f32_e32 v113, v113, v235
	v_sub_f32_e32 v114, v114, v235
	v_sub_f32_e32 v115, v115, v235
	v_sub_f32_e32 v116, v116, v235
	v_sub_f32_e32 v117, v117, v235
	v_sub_f32_e32 v118, v118, v235
	v_sub_f32_e32 v119, v119, v235
	v_sub_f32_e32 v120, v120, v235
	v_sub_f32_e32 v121, v121, v235
	v_sub_f32_e32 v122, v122, v235
	v_sub_f32_e32 v123, v123, v235
	v_sub_f32_e32 v124, v124, v235
	v_sub_f32_e32 v125, v125, v235
	v_sub_f32_e32 v126, v126, v235
	v_sub_f32_e32 v127, v127, v235
	v_mul_f32_e32 v233, v233, v237
	v_mul_f32_e32 v32, v32, v237
	v_mul_f32_e32 v33, v33, v237
	v_mul_f32_e32 v34, v34, v237
	v_mul_f32_e32 v35, v35, v237
	v_mul_f32_e32 v36, v36, v237
	v_mul_f32_e32 v37, v37, v237
	v_mul_f32_e32 v38, v38, v237
	v_mul_f32_e32 v39, v39, v237
	v_mul_f32_e32 v40, v40, v237
	v_mul_f32_e32 v41, v41, v237
	v_mul_f32_e32 v42, v42, v237
	v_mul_f32_e32 v43, v43, v237
	v_mul_f32_e32 v44, v44, v237
	v_mul_f32_e32 v45, v45, v237
	v_mul_f32_e32 v46, v46, v237
	v_mul_f32_e32 v47, v47, v237
	v_mul_f32_e32 v48, v48, v237
	v_mul_f32_e32 v49, v49, v237
	v_mul_f32_e32 v50, v50, v237
	v_mul_f32_e32 v51, v51, v237
	v_mul_f32_e32 v52, v52, v237
	v_mul_f32_e32 v53, v53, v237
	v_mul_f32_e32 v54, v54, v237
	v_mul_f32_e32 v55, v55, v237
	v_mul_f32_e32 v56, v56, v237
	v_mul_f32_e32 v57, v57, v237
	v_mul_f32_e32 v58, v58, v237
	v_mul_f32_e32 v59, v59, v237
	v_mul_f32_e32 v60, v60, v237
	v_mul_f32_e32 v61, v61, v237
	v_mul_f32_e32 v62, v62, v237
	v_mul_f32_e32 v63, v63, v237
	v_sub_f32_e32 v64, v64, v235
	v_sub_f32_e32 v80, v80, v235
	v_sub_f32_e32 v65, v65, v235
	v_sub_f32_e32 v81, v81, v235
	v_sub_f32_e32 v66, v66, v235
	v_sub_f32_e32 v82, v82, v235
	v_sub_f32_e32 v67, v67, v235
	v_sub_f32_e32 v83, v83, v235
	v_sub_f32_e32 v68, v68, v235
	v_sub_f32_e32 v84, v84, v235
	v_sub_f32_e32 v69, v69, v235
	v_sub_f32_e32 v85, v85, v235
	v_sub_f32_e32 v70, v70, v235
	v_sub_f32_e32 v86, v86, v235
	v_sub_f32_e32 v71, v71, v235
	v_sub_f32_e32 v87, v87, v235
	v_sub_f32_e32 v72, v72, v235
	v_sub_f32_e32 v88, v88, v235
	v_sub_f32_e32 v73, v73, v235
	v_sub_f32_e32 v89, v89, v235
	v_sub_f32_e32 v74, v74, v235
	v_sub_f32_e32 v90, v90, v235
	v_sub_f32_e32 v75, v75, v235
	v_sub_f32_e32 v91, v91, v235
	v_sub_f32_e32 v76, v76, v235
	v_sub_f32_e32 v92, v92, v235
	v_sub_f32_e32 v77, v77, v235
	v_sub_f32_e32 v93, v93, v235
	v_sub_f32_e32 v78, v78, v235
	v_sub_f32_e32 v94, v94, v235
	v_sub_f32_e32 v79, v79, v235
	v_sub_f32_e32 v95, v95, v235
	v_exp_f32_e32 v64, v64
	v_exp_f32_e32 v65, v65
	v_exp_f32_e32 v66, v66
	v_exp_f32_e32 v67, v67
	v_exp_f32_e32 v68, v68
	v_exp_f32_e32 v69, v69
	v_exp_f32_e32 v70, v70
	v_exp_f32_e32 v71, v71
	v_exp_f32_e32 v72, v72
	v_exp_f32_e32 v73, v73
	v_exp_f32_e32 v74, v74
	v_exp_f32_e32 v75, v75
	v_exp_f32_e32 v76, v76
	v_exp_f32_e32 v77, v77
	v_exp_f32_e32 v78, v78
	v_exp_f32_e32 v79, v79
	s_nop 0
	v_add_f32_e32 v231, v64, v65
	v_add_f32_e32 v231, v231, v66
	v_add_f32_e32 v231, v231, v67
	v_add_f32_e32 v231, v231, v68
	v_add_f32_e32 v231, v231, v69
	v_add_f32_e32 v231, v231, v70
	v_add_f32_e32 v231, v231, v71
	v_add_f32_e32 v231, v231, v72
	v_add_f32_e32 v231, v231, v73
	v_add_f32_e32 v231, v231, v74
	v_add_f32_e32 v231, v231, v75
	v_add_f32_e32 v231, v231, v76
	v_add_f32_e32 v231, v231, v77
	v_add_f32_e32 v231, v231, v78
	v_add_f32_e32 v231, v231, v79
	v_cvt_pk_f16_f32 v168, v64, v65
	v_cvt_pk_f16_f32 v169, v66, v67
	v_cvt_pk_f16_f32 v170, v68, v69
	v_cvt_pk_f16_f32 v171, v70, v71
	v_cvt_pk_f16_f32 v172, v72, v73
	v_cvt_pk_f16_f32 v173, v74, v75
	v_cvt_pk_f16_f32 v174, v76, v77
	v_cvt_pk_f16_f32 v175, v78, v79
	s_branch .Lovfret_b1_01
.Lovf_b1_10:
	s_waitcnt lgkmcnt(0)
	s_nop 15
	s_nop 15
	s_nop 15
	ds_read_b128 v[168:171], v225 offset:9216
	ds_read_b128 v[172:175], v225 offset:9248
	s_waitcnt lgkmcnt(0)
	v_mfma_f32_32x32x16_f16 v[80:95], v[168:171], v[144:147], v[112:127]
	v_mfma_f32_32x32x16_f16 v[80:95], v[172:175], v[148:151], v[80:95]
	s_nop 15
	ds_read_b128 v[168:171], v225 offset:9280
	ds_read_b128 v[172:175], v225 offset:9312
	s_waitcnt lgkmcnt(0)
	v_mfma_f32_32x32x16_f16 v[80:95], v[168:171], v[152:155], v[80:95]
	v_mfma_f32_32x32x16_f16 v[80:95], v[172:175], v[156:159], v[80:95]
	s_nop 15
	s_nop 15
	s_cmp_eq_u64 s[20:21], -1
	s_cbranch_scc1 .Lovfnm_b1_10
	v_lshrrev_b32_e64 v235, v234, s20
	v_bfe_u32 v236, v235, 0, 1
	v_cvt_f32_u32_e32 v236, v236
	v_sub_f32_e32 v236, 1.0, v236
	v_fmac_f32_e32 v80, s35, v236
	v_bfe_u32 v236, v235, 1, 1
	v_cvt_f32_u32_e32 v236, v236
	v_sub_f32_e32 v236, 1.0, v236
	v_fmac_f32_e32 v81, s35, v236
	v_bfe_u32 v236, v235, 2, 1
	v_cvt_f32_u32_e32 v236, v236
	v_sub_f32_e32 v236, 1.0, v236
	v_fmac_f32_e32 v82, s35, v236
	v_bfe_u32 v236, v235, 3, 1
	v_cvt_f32_u32_e32 v236, v236
	v_sub_f32_e32 v236, 1.0, v236
	v_fmac_f32_e32 v83, s35, v236
	v_bfe_u32 v236, v235, 8, 1
	v_cvt_f32_u32_e32 v236, v236
	v_sub_f32_e32 v236, 1.0, v236
	v_fmac_f32_e32 v84, s35, v236
	v_bfe_u32 v236, v235, 9, 1
	v_cvt_f32_u32_e32 v236, v236
	v_sub_f32_e32 v236, 1.0, v236
	v_fmac_f32_e32 v85, s35, v236
	v_bfe_u32 v236, v235, 10, 1
	v_cvt_f32_u32_e32 v236, v236
	v_sub_f32_e32 v236, 1.0, v236
	v_fmac_f32_e32 v86, s35, v236
	v_bfe_u32 v236, v235, 11, 1
	v_cvt_f32_u32_e32 v236, v236
	v_sub_f32_e32 v236, 1.0, v236
	v_fmac_f32_e32 v87, s35, v236
	v_bfe_u32 v236, v235, 16, 1
	v_cvt_f32_u32_e32 v236, v236
	v_sub_f32_e32 v236, 1.0, v236
	v_fmac_f32_e32 v88, s35, v236
	v_bfe_u32 v236, v235, 17, 1
	v_cvt_f32_u32_e32 v236, v236
	v_sub_f32_e32 v236, 1.0, v236
	v_fmac_f32_e32 v89, s35, v236
	v_bfe_u32 v236, v235, 18, 1
	v_cvt_f32_u32_e32 v236, v236
	v_sub_f32_e32 v236, 1.0, v236
	v_fmac_f32_e32 v90, s35, v236
	v_bfe_u32 v236, v235, 19, 1
	v_cvt_f32_u32_e32 v236, v236
	v_sub_f32_e32 v236, 1.0, v236
	v_fmac_f32_e32 v91, s35, v236
	v_bfe_u32 v236, v235, 24, 1
	v_cvt_f32_u32_e32 v236, v236
	v_sub_f32_e32 v236, 1.0, v236
	v_fmac_f32_e32 v92, s35, v236
	v_bfe_u32 v236, v235, 25, 1
	v_cvt_f32_u32_e32 v236, v236
	v_sub_f32_e32 v236, 1.0, v236
	v_fmac_f32_e32 v93, s35, v236
	v_bfe_u32 v236, v235, 26, 1
	v_cvt_f32_u32_e32 v236, v236
	v_sub_f32_e32 v236, 1.0, v236
	v_fmac_f32_e32 v94, s35, v236
	v_bfe_u32 v236, v235, 27, 1
	v_cvt_f32_u32_e32 v236, v236
	v_sub_f32_e32 v236, 1.0, v236
	v_fmac_f32_e32 v95, s35, v236

.Lovf_b1_11:
	s_waitcnt lgkmcnt(0)
	s_nop 15
	s_nop 15
	s_nop 15
	ds_read_b128 v[160:163], v225 offset:13824
	ds_read_b128 v[164:167], v225 offset:13856
	s_waitcnt lgkmcnt(0)
	v_mfma_f32_32x32x16_f16 v[64:79], v[160:163], v[144:147], v[112:127]
	v_mfma_f32_32x32x16_f16 v[64:79], v[164:167], v[148:151], v[64:79]
	s_nop 15
	ds_read_b128 v[160:163], v225 offset:13888
	ds_read_b128 v[164:167], v225 offset:13920
	s_waitcnt lgkmcnt(0)
	v_mfma_f32_32x32x16_f16 v[64:79], v[160:163], v[152:155], v[64:79]
	v_mfma_f32_32x32x16_f16 v[64:79], v[164:167], v[156:159], v[64:79]
	s_nop 15
	s_nop 15
	s_cmp_eq_u64 s[20:21], -1
	s_cbranch_scc1 .Lovfnm_b1_11
	v_lshrrev_b32_e64 v235, v234, s21
	v_bfe_u32 v236, v235, 0, 1
	v_cvt_f32_u32_e32 v236, v236
	v_sub_f32_e32 v236, 1.0, v236
	v_fmac_f32_e32 v64, s35, v236
	v_bfe_u32 v236, v235, 1, 1
	v_cvt_f32_u32_e32 v236, v236
	v_sub_f32_e32 v236, 1.0, v236
	v_fmac_f32_e32 v65, s35, v236
	v_bfe_u32 v236, v235, 2, 1
	v_cvt_f32_u32_e32 v236, v236
	v_sub_f32_e32 v236, 1.0, v236
	v_fmac_f32_e32 v66, s35, v236
	v_bfe_u32 v236, v235, 3, 1
	v_cvt_f32_u32_e32 v236, v236
	v_sub_f32_e32 v236, 1.0, v236
	v_fmac_f32_e32 v67, s35, v236
	v_bfe_u32 v236, v235, 8, 1
	v_cvt_f32_u32_e32 v236, v236
	v_sub_f32_e32 v236, 1.0, v236
	v_fmac_f32_e32 v68, s35, v236
	v_bfe_u32 v236, v235, 9, 1
	v_cvt_f32_u32_e32 v236, v236
	v_sub_f32_e32 v236, 1.0, v236
	v_fmac_f32_e32 v69, s35, v236
	v_bfe_u32 v236, v235, 10, 1
	v_cvt_f32_u32_e32 v236, v236
	v_sub_f32_e32 v236, 1.0, v236
	v_fmac_f32_e32 v70, s35, v236
	v_bfe_u32 v236, v235, 11, 1
	v_cvt_f32_u32_e32 v236, v236
	v_sub_f32_e32 v236, 1.0, v236
	v_fmac_f32_e32 v71, s35, v236
	v_bfe_u32 v236, v235, 16, 1
	v_cvt_f32_u32_e32 v236, v236
	v_sub_f32_e32 v236, 1.0, v236
	v_fmac_f32_e32 v72, s35, v236
	v_bfe_u32 v236, v235, 17, 1
	v_cvt_f32_u32_e32 v236, v236
	v_sub_f32_e32 v236, 1.0, v236
	v_fmac_f32_e32 v73, s35, v236
	v_bfe_u32 v236, v235, 18, 1
	v_cvt_f32_u32_e32 v236, v236
	v_sub_f32_e32 v236, 1.0, v236
	v_fmac_f32_e32 v74, s35, v236
	v_bfe_u32 v236, v235, 19, 1
	v_cvt_f32_u32_e32 v236, v236
	v_sub_f32_e32 v236, 1.0, v236
	v_fmac_f32_e32 v75, s35, v236
	v_bfe_u32 v236, v235, 24, 1
	v_cvt_f32_u32_e32 v236, v236
	v_sub_f32_e32 v236, 1.0, v236
	v_fmac_f32_e32 v76, s35, v236
	v_bfe_u32 v236, v235, 25, 1
	v_cvt_f32_u32_e32 v236, v236
	v_sub_f32_e32 v236, 1.0, v236
	v_fmac_f32_e32 v77, s35, v236
	v_bfe_u32 v236, v235, 26, 1
	v_cvt_f32_u32_e32 v236, v236
	v_sub_f32_e32 v236, 1.0, v236
	v_fmac_f32_e32 v78, s35, v236
	v_bfe_u32 v236, v235, 27, 1
	v_cvt_f32_u32_e32 v236, v236
	v_sub_f32_e32 v236, 1.0, v236
	v_fmac_f32_e32 v79, s35, v236

.Lovf_b1_20:
	s_waitcnt lgkmcnt(0)
	s_nop 15
	s_nop 15
	s_nop 15
	ds_read_b128 v[168:171], v225 offset:18432
	ds_read_b128 v[172:175], v225 offset:18464
	s_waitcnt lgkmcnt(0)
	v_mfma_f32_32x32x16_f16 v[80:95], v[168:171], v[144:147], v[112:127]
	v_mfma_f32_32x32x16_f16 v[80:95], v[172:175], v[148:151], v[80:95]
	s_nop 15
	ds_read_b128 v[168:171], v225 offset:18496
	ds_read_b128 v[172:175], v225 offset:18528
	s_waitcnt lgkmcnt(0)
	v_mfma_f32_32x32x16_f16 v[80:95], v[168:171], v[152:155], v[80:95]
	v_mfma_f32_32x32x16_f16 v[80:95], v[172:175], v[156:159], v[80:95]
	s_nop 15
	s_nop 15
	s_cmp_eq_u64 s[20:21], -1
	s_cbranch_scc1 .Lovfnm_b1_20
	v_lshrrev_b32_e64 v235, v234, s20
	v_bfe_u32 v236, v235, 0, 1
	v_cvt_f32_u32_e32 v236, v236
	v_sub_f32_e32 v236, 1.0, v236
	v_fmac_f32_e32 v80, s35, v236
	v_bfe_u32 v236, v235, 1, 1
	v_cvt_f32_u32_e32 v236, v236
	v_sub_f32_e32 v236, 1.0, v236
	v_fmac_f32_e32 v81, s35, v236
	v_bfe_u32 v236, v235, 2, 1
	v_cvt_f32_u32_e32 v236, v236
	v_sub_f32_e32 v236, 1.0, v236
	v_fmac_f32_e32 v82, s35, v236
	v_bfe_u32 v236, v235, 3, 1
	v_cvt_f32_u32_e32 v236, v236
	v_sub_f32_e32 v236, 1.0, v236
	v_fmac_f32_e32 v83, s35, v236
	v_bfe_u32 v236, v235, 8, 1
	v_cvt_f32_u32_e32 v236, v236
	v_sub_f32_e32 v236, 1.0, v236
	v_fmac_f32_e32 v84, s35, v236
	v_bfe_u32 v236, v235, 9, 1
	v_cvt_f32_u32_e32 v236, v236
	v_sub_f32_e32 v236, 1.0, v236
	v_fmac_f32_e32 v85, s35, v236
	v_bfe_u32 v236, v235, 10, 1
	v_cvt_f32_u32_e32 v236, v236
	v_sub_f32_e32 v236, 1.0, v236
	v_fmac_f32_e32 v86, s35, v236
	v_bfe_u32 v236, v235, 11, 1
	v_cvt_f32_u32_e32 v236, v236
	v_sub_f32_e32 v236, 1.0, v236
	v_fmac_f32_e32 v87, s35, v236
	v_bfe_u32 v236, v235, 16, 1
	v_cvt_f32_u32_e32 v236, v236
	v_sub_f32_e32 v236, 1.0, v236
	v_fmac_f32_e32 v88, s35, v236
	v_bfe_u32 v236, v235, 17, 1
	v_cvt_f32_u32_e32 v236, v236
	v_sub_f32_e32 v236, 1.0, v236
	v_fmac_f32_e32 v89, s35, v236
	v_bfe_u32 v236, v235, 18, 1
	v_cvt_f32_u32_e32 v236, v236
	v_sub_f32_e32 v236, 1.0, v236
	v_fmac_f32_e32 v90, s35, v236
	v_bfe_u32 v236, v235, 19, 1
	v_cvt_f32_u32_e32 v236, v236
	v_sub_f32_e32 v236, 1.0, v236
	v_fmac_f32_e32 v91, s35, v236
	v_bfe_u32 v236, v235, 24, 1
	v_cvt_f32_u32_e32 v236, v236
	v_sub_f32_e32 v236, 1.0, v236
	v_fmac_f32_e32 v92, s35, v236
	v_bfe_u32 v236, v235, 25, 1
	v_cvt_f32_u32_e32 v236, v236
	v_sub_f32_e32 v236, 1.0, v236
	v_fmac_f32_e32 v93, s35, v236
	v_bfe_u32 v236, v235, 26, 1
	v_cvt_f32_u32_e32 v236, v236
	v_sub_f32_e32 v236, 1.0, v236
	v_fmac_f32_e32 v94, s35, v236
	v_bfe_u32 v236, v235, 27, 1
	v_cvt_f32_u32_e32 v236, v236
	v_sub_f32_e32 v236, 1.0, v236
	v_fmac_f32_e32 v95, s35, v236

.Lovf_b1_21:
	s_waitcnt lgkmcnt(0)
	s_nop 15
	s_nop 15
	s_nop 15
	ds_read_b128 v[160:163], v225 offset:23040
	ds_read_b128 v[164:167], v225 offset:23072
	s_waitcnt lgkmcnt(0)
	v_mfma_f32_32x32x16_f16 v[64:79], v[160:163], v[144:147], v[112:127]
	v_mfma_f32_32x32x16_f16 v[64:79], v[164:167], v[148:151], v[64:79]
	s_nop 15
	ds_read_b128 v[160:163], v225 offset:23104
	ds_read_b128 v[164:167], v225 offset:23136
	s_waitcnt lgkmcnt(0)
	v_mfma_f32_32x32x16_f16 v[64:79], v[160:163], v[152:155], v[64:79]
	v_mfma_f32_32x32x16_f16 v[64:79], v[164:167], v[156:159], v[64:79]
	s_nop 15
	s_nop 15
	s_cmp_eq_u64 s[20:21], -1
	s_cbranch_scc1 .Lovfnm_b1_21
	v_lshrrev_b32_e64 v235, v234, s21
	v_bfe_u32 v236, v235, 0, 1
	v_cvt_f32_u32_e32 v236, v236
	v_sub_f32_e32 v236, 1.0, v236
	v_fmac_f32_e32 v64, s35, v236
	v_bfe_u32 v236, v235, 1, 1
	v_cvt_f32_u32_e32 v236, v236
	v_sub_f32_e32 v236, 1.0, v236
	v_fmac_f32_e32 v65, s35, v236
	v_bfe_u32 v236, v235, 2, 1
	v_cvt_f32_u32_e32 v236, v236
	v_sub_f32_e32 v236, 1.0, v236
	v_fmac_f32_e32 v66, s35, v236
	v_bfe_u32 v236, v235, 3, 1
	v_cvt_f32_u32_e32 v236, v236
	v_sub_f32_e32 v236, 1.0, v236
	v_fmac_f32_e32 v67, s35, v236
	v_bfe_u32 v236, v235, 8, 1
	v_cvt_f32_u32_e32 v236, v236
	v_sub_f32_e32 v236, 1.0, v236
	v_fmac_f32_e32 v68, s35, v236
	v_bfe_u32 v236, v235, 9, 1
	v_cvt_f32_u32_e32 v236, v236
	v_sub_f32_e32 v236, 1.0, v236
	v_fmac_f32_e32 v69, s35, v236
	v_bfe_u32 v236, v235, 10, 1
	v_cvt_f32_u32_e32 v236, v236
	v_sub_f32_e32 v236, 1.0, v236
	v_fmac_f32_e32 v70, s35, v236
	v_bfe_u32 v236, v235, 11, 1
	v_cvt_f32_u32_e32 v236, v236
	v_sub_f32_e32 v236, 1.0, v236
	v_fmac_f32_e32 v71, s35, v236
	v_bfe_u32 v236, v235, 16, 1
	v_cvt_f32_u32_e32 v236, v236
	v_sub_f32_e32 v236, 1.0, v236
	v_fmac_f32_e32 v72, s35, v236
	v_bfe_u32 v236, v235, 17, 1
	v_cvt_f32_u32_e32 v236, v236
	v_sub_f32_e32 v236, 1.0, v236
	v_fmac_f32_e32 v73, s35, v236
	v_bfe_u32 v236, v235, 18, 1
	v_cvt_f32_u32_e32 v236, v236
	v_sub_f32_e32 v236, 1.0, v236
	v_fmac_f32_e32 v74, s35, v236
	v_bfe_u32 v236, v235, 19, 1
	v_cvt_f32_u32_e32 v236, v236
	v_sub_f32_e32 v236, 1.0, v236
	v_fmac_f32_e32 v75, s35, v236
	v_bfe_u32 v236, v235, 24, 1
	v_cvt_f32_u32_e32 v236, v236
	v_sub_f32_e32 v236, 1.0, v236
	v_fmac_f32_e32 v76, s35, v236
	v_bfe_u32 v236, v235, 25, 1
	v_cvt_f32_u32_e32 v236, v236
	v_sub_f32_e32 v236, 1.0, v236
	v_fmac_f32_e32 v77, s35, v236
	v_bfe_u32 v236, v235, 26, 1
	v_cvt_f32_u32_e32 v236, v236
	v_sub_f32_e32 v236, 1.0, v236
	v_fmac_f32_e32 v78, s35, v236
	v_bfe_u32 v236, v235, 27, 1
	v_cvt_f32_u32_e32 v236, v236
	v_sub_f32_e32 v236, 1.0, v236
	v_fmac_f32_e32 v79, s35, v236

.Lovf_b1_30:
	s_waitcnt lgkmcnt(0)
	s_nop 15
	s_nop 15
	s_nop 15
	ds_read_b128 v[168:171], v225 offset:27648
	ds_read_b128 v[172:175], v225 offset:27680
	s_waitcnt lgkmcnt(0)
	v_mfma_f32_32x32x16_f16 v[80:95], v[168:171], v[144:147], v[112:127]
	v_mfma_f32_32x32x16_f16 v[80:95], v[172:175], v[148:151], v[80:95]
	s_nop 15
	ds_read_b128 v[168:171], v225 offset:27712
	ds_read_b128 v[172:175], v225 offset:27744
	s_waitcnt lgkmcnt(0)
	v_mfma_f32_32x32x16_f16 v[80:95], v[168:171], v[152:155], v[80:95]
	v_mfma_f32_32x32x16_f16 v[80:95], v[172:175], v[156:159], v[80:95]
	s_nop 15
	s_nop 15
	s_cmp_eq_u64 s[20:21], -1
	s_cbranch_scc1 .Lovfnm_b1_30
	v_lshrrev_b32_e64 v235, v234, s20
	v_bfe_u32 v236, v235, 0, 1
	v_cvt_f32_u32_e32 v236, v236
	v_sub_f32_e32 v236, 1.0, v236
	v_fmac_f32_e32 v80, s35, v236
	v_bfe_u32 v236, v235, 1, 1
	v_cvt_f32_u32_e32 v236, v236
	v_sub_f32_e32 v236, 1.0, v236
	v_fmac_f32_e32 v81, s35, v236
	v_bfe_u32 v236, v235, 2, 1
	v_cvt_f32_u32_e32 v236, v236
	v_sub_f32_e32 v236, 1.0, v236
	v_fmac_f32_e32 v82, s35, v236
	v_bfe_u32 v236, v235, 3, 1
	v_cvt_f32_u32_e32 v236, v236
	v_sub_f32_e32 v236, 1.0, v236
	v_fmac_f32_e32 v83, s35, v236
	v_bfe_u32 v236, v235, 8, 1
	v_cvt_f32_u32_e32 v236, v236
	v_sub_f32_e32 v236, 1.0, v236
	v_fmac_f32_e32 v84, s35, v236
	v_bfe_u32 v236, v235, 9, 1
	v_cvt_f32_u32_e32 v236, v236
	v_sub_f32_e32 v236, 1.0, v236
	v_fmac_f32_e32 v85, s35, v236
	v_bfe_u32 v236, v235, 10, 1
	v_cvt_f32_u32_e32 v236, v236
	v_sub_f32_e32 v236, 1.0, v236
	v_fmac_f32_e32 v86, s35, v236
	v_bfe_u32 v236, v235, 11, 1
	v_cvt_f32_u32_e32 v236, v236
	v_sub_f32_e32 v236, 1.0, v236
	v_fmac_f32_e32 v87, s35, v236
	v_bfe_u32 v236, v235, 16, 1
	v_cvt_f32_u32_e32 v236, v236
	v_sub_f32_e32 v236, 1.0, v236
	v_fmac_f32_e32 v88, s35, v236
	v_bfe_u32 v236, v235, 17, 1
	v_cvt_f32_u32_e32 v236, v236
	v_sub_f32_e32 v236, 1.0, v236
	v_fmac_f32_e32 v89, s35, v236
	v_bfe_u32 v236, v235, 18, 1
	v_cvt_f32_u32_e32 v236, v236
	v_sub_f32_e32 v236, 1.0, v236
	v_fmac_f32_e32 v90, s35, v236
	v_bfe_u32 v236, v235, 19, 1
	v_cvt_f32_u32_e32 v236, v236
	v_sub_f32_e32 v236, 1.0, v236
	v_fmac_f32_e32 v91, s35, v236
	v_bfe_u32 v236, v235, 24, 1
	v_cvt_f32_u32_e32 v236, v236
	v_sub_f32_e32 v236, 1.0, v236
	v_fmac_f32_e32 v92, s35, v236
	v_bfe_u32 v236, v235, 25, 1
	v_cvt_f32_u32_e32 v236, v236
	v_sub_f32_e32 v236, 1.0, v236
	v_fmac_f32_e32 v93, s35, v236
	v_bfe_u32 v236, v235, 26, 1
	v_cvt_f32_u32_e32 v236, v236
	v_sub_f32_e32 v236, 1.0, v236
	v_fmac_f32_e32 v94, s35, v236
	v_bfe_u32 v236, v235, 27, 1
	v_cvt_f32_u32_e32 v236, v236
	v_sub_f32_e32 v236, 1.0, v236
	v_fmac_f32_e32 v95, s35, v236

.Lovf_b1_31:
	s_waitcnt lgkmcnt(0)
	s_nop 15
	s_nop 15
	s_nop 15
	ds_read_b128 v[160:163], v225 offset:32256
	ds_read_b128 v[164:167], v225 offset:32288
	s_waitcnt lgkmcnt(0)
	v_mfma_f32_32x32x16_f16 v[64:79], v[160:163], v[144:147], v[112:127]
	v_mfma_f32_32x32x16_f16 v[64:79], v[164:167], v[148:151], v[64:79]
	s_nop 15
	ds_read_b128 v[160:163], v225 offset:32320
	ds_read_b128 v[164:167], v225 offset:32352
	s_waitcnt lgkmcnt(0)
	v_mfma_f32_32x32x16_f16 v[64:79], v[160:163], v[152:155], v[64:79]
	v_mfma_f32_32x32x16_f16 v[64:79], v[164:167], v[156:159], v[64:79]
	s_nop 15
	s_nop 15
	s_cmp_eq_u64 s[20:21], -1
	s_cbranch_scc1 .Lovfnm_b1_31
	v_lshrrev_b32_e64 v235, v234, s21
	v_bfe_u32 v236, v235, 0, 1
	v_cvt_f32_u32_e32 v236, v236
	v_sub_f32_e32 v236, 1.0, v236
	v_fmac_f32_e32 v64, s35, v236
	v_bfe_u32 v236, v235, 1, 1
	v_cvt_f32_u32_e32 v236, v236
	v_sub_f32_e32 v236, 1.0, v236
	v_fmac_f32_e32 v65, s35, v236
	v_bfe_u32 v236, v235, 2, 1
	v_cvt_f32_u32_e32 v236, v236
	v_sub_f32_e32 v236, 1.0, v236
	v_fmac_f32_e32 v66, s35, v236
	v_bfe_u32 v236, v235, 3, 1
	v_cvt_f32_u32_e32 v236, v236
	v_sub_f32_e32 v236, 1.0, v236
	v_fmac_f32_e32 v67, s35, v236
	v_bfe_u32 v236, v235, 8, 1
	v_cvt_f32_u32_e32 v236, v236
	v_sub_f32_e32 v236, 1.0, v236
	v_fmac_f32_e32 v68, s35, v236
	v_bfe_u32 v236, v235, 9, 1
	v_cvt_f32_u32_e32 v236, v236
	v_sub_f32_e32 v236, 1.0, v236
	v_fmac_f32_e32 v69, s35, v236
	v_bfe_u32 v236, v235, 10, 1
	v_cvt_f32_u32_e32 v236, v236
	v_sub_f32_e32 v236, 1.0, v236
	v_fmac_f32_e32 v70, s35, v236
	v_bfe_u32 v236, v235, 11, 1
	v_cvt_f32_u32_e32 v236, v236
	v_sub_f32_e32 v236, 1.0, v236
	v_fmac_f32_e32 v71, s35, v236
	v_bfe_u32 v236, v235, 16, 1
	v_cvt_f32_u32_e32 v236, v236
	v_sub_f32_e32 v236, 1.0, v236
	v_fmac_f32_e32 v72, s35, v236
	v_bfe_u32 v236, v235, 17, 1
	v_cvt_f32_u32_e32 v236, v236
	v_sub_f32_e32 v236, 1.0, v236
	v_fmac_f32_e32 v73, s35, v236
	v_bfe_u32 v236, v235, 18, 1
	v_cvt_f32_u32_e32 v236, v236
	v_sub_f32_e32 v236, 1.0, v236
	v_fmac_f32_e32 v74, s35, v236
	v_bfe_u32 v236, v235, 19, 1
	v_cvt_f32_u32_e32 v236, v236
	v_sub_f32_e32 v236, 1.0, v236
	v_fmac_f32_e32 v75, s35, v236
	v_bfe_u32 v236, v235, 24, 1
	v_cvt_f32_u32_e32 v236, v236
	v_sub_f32_e32 v236, 1.0, v236
	v_fmac_f32_e32 v76, s35, v236
	v_bfe_u32 v236, v235, 25, 1
	v_cvt_f32_u32_e32 v236, v236
	v_sub_f32_e32 v236, 1.0, v236
	v_fmac_f32_e32 v77, s35, v236
	v_bfe_u32 v236, v235, 26, 1
	v_cvt_f32_u32_e32 v236, v236
	v_sub_f32_e32 v236, 1.0, v236
	v_fmac_f32_e32 v78, s35, v236
	v_bfe_u32 v236, v235, 27, 1
	v_cvt_f32_u32_e32 v236, v236
	v_sub_f32_e32 v236, 1.0, v236
	v_fmac_f32_e32 v79, s35, v236
